# de-serialized prologue scale+silu loops, norm2 router LDS fill, in-proj epilogue scale loads (8 loads in flight instead of 1)
# baseline (speedup 1.0000x reference)
;     template <class AT> __device__ __forceinline__ void operator()(const AT (&acc)[2][2][4][2], const Unit& u, int wr, int wc, int fr, int fq) const {
;         const int row0 = u.pm * BM + wr * 64 + fr, col0 = u.pn * BM + wc * 32 + 8 * fq;
;         const int pt = u.pm % 17;
;         bf16_t* const O = (bf16_t*)(wsb + WS_R2); const float* const sa = (const float*)(wsb + WS_SAX);
;         unsigned char* const k8a = wsb + WS_K8; unsigned char* const k8b = wsb + WS_K8D; unsigned char* const v8a = wsb + WS_V8; unsigned char* const v8b = wsb + WS_V8D;
;         int frl = fr, fql = fq; asm volatile("" : "+v"(frl), "+v"(fql));
;         unsigned char* kq = nullptr;
;         if (rope) { if (u.pn == 4) kq = k8a; else if (u.pn >= 10 && u.pn <= 13) kq = k8b + (size_t)(u.pn - 10) * 2 * NROWS * 128; }
;         if (u.pn == 5 || (rope && u.pn >= 14)) {
;             const int b = u.pm / 17, qi = frl & 3, a4 = frl >> 2, nhv = u.pn == 5 ? 2 : 8, hv0 = u.pn == 5 ? 0 : (u.pn - 14) * 2; unsigned char* vq = u.pn == 5 ? v8a : v8b;
;             const unsigned sel = (unsigned)qi | ((unsigned)(4 + qi) << 8) | 0x0c0c0000u;
; #pragma unroll
;             for (int ai = 0; ai < 2; ++ai)
; #pragma unroll
;                 for (int m = 0; m < 4; ++m) { const float rsc = sa[row0 + ai * HALF + m * 16] * sw;
;                     const int tile = (u.pm % 17) * 4 + wr + 2 * ai, pos0 = 32 * (a4 & 1) + 16 * (m >> 1) + 4 * ((2 * m + (a4 >> 1)) & 3);
; #pragma unroll
;                     for (int bj = 0; bj < 2; ++bj) { const f32x4 v0 = tof(acc[ai][bj][m][0]) * rsc, v1 = tof(acc[ai][bj][m][1]) * rsc;
;                         unsigned char* tb_ = vq + ((size_t)((b * nhv + hv0 + bj) * 68 + tile)) * 8192 + (size_t)(wc * 32 + 8 * fql) * 64 + pos0;
; #pragma unroll
;                         for (int hh = 0; hh < 2; ++hh) { const f32x4 vv = hh ? v1 : v0; const int w = (int)pack_f8x4(vv[0], vv[1], vv[2], vv[3], 1.f);
;                             const unsigned p0 = (unsigned)__builtin_amdgcn_update_dpp(0, w, 0x00, 0xf, 0xf, false), p1 = (unsigned)__builtin_amdgcn_update_dpp(0, w, 0x55, 0xf, 0xf, false);
;                             const unsigned p2 = (unsigned)__builtin_amdgcn_update_dpp(0, w, 0xaa, 0xf, 0xf, false), p3 = (unsigned)__builtin_amdgcn_update_dpp(0, w, 0xff, 0xf, 0xf, false);
.LBB0_248:
	s_mul_hi_i32 s17, s26, 0x78787879
	s_lshr_b32 s19, s17, 31
	s_ashr_i32 s17, s17, 3
	s_add_i32 s17, s17, s19
	s_lshl_b32 s31, s26, 8
	s_mul_i32 s19, s17, 17
	s_add_i32 s31, s31, s73
	s_sub_i32 s19, s26, s19
	s_cmp_eq_u32 s24, 5
	s_cselect_b64 s[26:27], -1, 0
	v_or_b32_e32 v152, s31, v185
	s_and_b64 vcc, exec, s[26:27]
	s_cbranch_vccnz .LBB0_256
	s_cmp_lt_i32 s24, 14
	v_readlane_b32 s44, v254, 31
	s_cselect_b64 s[40:41], -1, 0
	v_readlane_b32 s45, v254, 32
	s_or_b64 s[40:41], s[44:45], s[40:41]
	s_mov_b64 s[28:29], -1
	s_and_b64 vcc, exec, s[40:41]
	s_cbranch_vccz .LBB0_350
	v_ashrrev_i32_e32 v153, 31, v152
	v_lshl_add_u64 v[162:163], v[152:153], 2, s[12:13]
	global_load_dword v224, v[162:163], off
	global_load_dword v225, v[162:163], off offset:64
	global_load_dword v226, v[162:163], off offset:128
	global_load_dword v227, v[162:163], off offset:192
	global_load_dword v228, v[162:163], off offset:512
	global_load_dword v229, v[162:163], off offset:576
	global_load_dword v230, v[162:163], off offset:640
	global_load_dword v231, v[162:163], off offset:704
	s_cmp_lg_u32 s19, 0
	s_cselect_b64 s[28:29], -1, 0
	s_cmp_lt_i32 s24, 14
	s_cselect_b64 s[40:41], -1, 0
	s_and_b64 s[28:29], s[48:49], s[28:29]
	s_and_b64 s[28:29], s[28:29], s[40:41]
	s_lshl_b32 s25, s19, 8
	s_add_i32 s25, s82, s25
	v_mov_b32_e32 v154, 0
	v_cndmask_b32_e64 v1, 0, 1, s[28:29]
	s_ashr_i32 s30, s25, 6
	v_cmp_ne_u32_e64 s[40:41], 1, v1
	s_andn2_b64 vcc, exec, s[28:29]
	v_mov_b32_e32 v155, v154
	v_mov_b32_e32 v204, v154
	v_mov_b32_e32 v161, v154
	v_mov_b32_e32 v156, v154
	v_mov_b32_e32 v157, v154
	v_mov_b32_e32 v153, v154
	v_mov_b32_e32 v159, v154
	s_cbranch_vccnz .LBB0_252
	v_mov_b32_e32 v1, s30
	v_cndmask_b32_e64 v1, v185, v1, s[36:37]
	v_cvt_f32_i32_e32 v1, v1
	v_mul_f32_e32 v133, v191, v1
	v_mul_f32_e32 v133, 0.15915494, v133
	v_mul_f32_e32 v134, v192, v1
	v_cos_f32_e32 v156, v133
	v_sin_f32_e32 v154, v133
	v_mul_f32_e32 v133, v193, v1
	v_mul_f32_e32 v1, v194, v1
	v_mul_f32_e32 v134, 0.15915494, v134
	v_mul_f32_e32 v133, 0.15915494, v133
	v_mul_f32_e32 v1, 0.15915494, v1
	v_cos_f32_e32 v157, v134
	v_sin_f32_e32 v155, v134
	v_cos_f32_e32 v153, v133
	v_sin_f32_e32 v204, v133
	v_cos_f32_e32 v159, v1
	v_sin_f32_e32 v161, v1
.LBB0_252:
	v_cvt_f32_i32_e32 v135, v131
	v_cvt_f32_i32_e32 v134, v130
	s_waitcnt vmcnt(0)
	v_mov_b32_e32 v132, v224
	v_mul_f32_e32 v170, v184, v132
	v_cvt_f32_i32_e32 v133, v129
	v_cvt_f32_i32_e32 v132, v128
	v_pk_mul_f32 v[168:169], v[170:171], v[134:135] op_sel_hi:[0,1]
	v_cvt_f32_i32_e32 v135, v127
	v_cvt_f32_i32_e32 v134, v126
	v_cvt_f32_i32_e32 v165, v125
	v_cvt_f32_i32_e32 v164, v124
	v_pk_mul_f32 v[178:179], v[170:171], v[132:133] op_sel_hi:[0,1]
	v_pk_mul_f32 v[174:175], v[170:171], v[134:135] op_sel_hi:[0,1]
	s_and_b64 vcc, exec, s[40:41]
	v_pk_mul_f32 v[176:177], v[170:171], v[164:165] op_sel_hi:[0,1]
	s_cbranch_vccnz .LBB0_254
	v_pk_mul_f32 v[134:135], v[176:177], v[156:157]
	v_mul_f32_e32 v164, v174, v204
	v_mul_f32_e32 v166, v174, v153
	v_mov_b32_e32 v174, v169
	v_mov_b32_e32 v160, v159
	v_pk_mul_f32 v[132:133], v[176:177], v[154:155]
	v_pk_fma_f32 v[176:177], v[178:179], v[154:155], v[134:135]
	v_mul_f32_e32 v134, v168, v153
	v_mul_f32_e32 v172, v168, v204
	v_pk_mul_f32 v[168:169], v[174:175], v[160:161]
	v_mov_b32_e32 v158, v161
	v_mov_b32_e32 v135, v168
	v_mov_b32_e32 v165, v169
	v_pk_add_f32 v[168:169], v[134:135], v[164:165] neg_lo:[0,1] neg_hi:[0,1]
	v_pk_mul_f32 v[134:135], v[174:175], v[158:159]
	v_pk_fma_f32 v[132:133], v[178:179], v[156:157], v[132:133] neg_lo:[0,0,1] neg_hi:[0,0,1]
	v_mov_b32_e32 v173, v134
	v_mov_b32_e32 v167, v135
	v_pk_add_f32 v[174:175], v[172:173], v[166:167]
	v_mov_b32_e32 v178, v132
	v_mov_b32_e32 v179, v133

; __device__ __forceinline__ f32x4 tof(const i32x4& a) { return (f32x4){(float)a.x, (float)a.y, (float)a.z, (float)a.w}; }
;     template <class AT> __device__ __forceinline__ void operator()(const AT (&acc)[2][2][4][2], const Unit& u, int wr, int wc, int fr, int fq) const {
;     ...
;         for (int ai = 0; ai < 2; ++ai)
; #pragma unroll
;             for (int m = 0; m < 4; ++m) { bf16_t* rowp = O + (size_t)(row0 + ai * HALF + m * 16) * INW + col0; const float rsc = sa[row0 + ai * HALF + m * 16] * sw;
;                 float cs[4], sn[4];
;                 if (dorope) { const int pos = (pt - 1) * 256 + wr * 64 + ai * HALF + m * 16 + fr; const float pp = (float)((wc >> 1) == 0 ? (pos >> 6) : (pos & 63));
; #pragma unroll
;                     for (int i = 0; i < 4; ++i) { const float ang = pp * inv[i]; cs[i] = __cosf(ang); sn[i] = __sinf(ang); } }
; #pragma unroll
;                 for (int bj = 0; bj < 2; ++bj) { f32x4 v0 = tof(acc[ai][bj][m][0]) * rsc, v1 = tof(acc[ai][bj][m][1]) * rsc;
;                     if (dorope) {
; #pragma unroll
;                         for (int i = 0; i < 4; ++i) { const float a = v0[i], b = v1[i]; v0[i] = a * cs[i] - b * sn[i]; v1[i] = b * cs[i] + a * sn[i]; } }
.LBB0_265:
	v_or_b32_e32 v170, 16, v152
	v_ashrrev_i32_e32 v171, 31, v170
	v_lshl_add_u64 v[132:133], v[170:171], 2, s[12:13]
	s_and_b64 vcc, exec, s[40:41]
	s_cbranch_vccnz .LBB0_267
	v_mov_b32_e32 v1, s30
	v_cndmask_b32_e64 v1, v187, v1, s[36:37]
	v_cvt_f32_i32_e32 v1, v1
	v_mul_f32_e32 v133, v191, v1
	v_mul_f32_e32 v133, 0.15915494, v133
	v_mul_f32_e32 v134, v192, v1
	v_cos_f32_e32 v156, v133
	v_sin_f32_e32 v154, v133
	v_mul_f32_e32 v133, v193, v1
	v_mul_f32_e32 v1, v194, v1
	v_mul_f32_e32 v134, 0.15915494, v134
	v_mul_f32_e32 v133, 0.15915494, v133
	v_mul_f32_e32 v1, 0.15915494, v1
	v_cos_f32_e32 v157, v134
	v_sin_f32_e32 v155, v134
	v_cos_f32_e32 v153, v133
	v_sin_f32_e32 v204, v133
	v_cos_f32_e32 v159, v1
	v_sin_f32_e32 v161, v1
.LBB0_267:
	v_cvt_f32_i32_e32 v135, v115
	v_cvt_f32_i32_e32 v134, v114
	v_mov_b32_e32 v132, v225
	v_mul_f32_e32 v172, v184, v132
	v_cvt_f32_i32_e32 v133, v113
	v_cvt_f32_i32_e32 v132, v112
	v_pk_mul_f32 v[176:177], v[172:173], v[134:135] op_sel_hi:[0,1]
	v_cvt_f32_i32_e32 v135, v111
	v_cvt_f32_i32_e32 v134, v110
	v_cvt_f32_i32_e32 v175, v109
	v_cvt_f32_i32_e32 v174, v108
	v_pk_mul_f32 v[182:183], v[172:173], v[132:133] op_sel_hi:[0,1]
	v_pk_mul_f32 v[178:179], v[172:173], v[134:135] op_sel_hi:[0,1]
	s_and_b64 vcc, exec, s[40:41]
	v_pk_mul_f32 v[180:181], v[172:173], v[174:175] op_sel_hi:[0,1]
	s_cbranch_vccnz .LBB0_269
	v_pk_mul_f32 v[132:133], v[180:181], v[154:155]
	v_pk_mul_f32 v[134:135], v[180:181], v[156:157]
	v_pk_fma_f32 v[132:133], v[182:183], v[156:157], v[132:133] neg_lo:[0,0,1] neg_hi:[0,0,1]
	v_pk_fma_f32 v[180:181], v[182:183], v[154:155], v[134:135]
	v_mul_f32_e32 v174, v178, v204
	v_mul_f32_e32 v182, v178, v153
	v_mov_b32_e32 v178, v177
	v_mov_b32_e32 v160, v159
	v_mul_f32_e32 v134, v176, v153
	v_mul_f32_e32 v198, v176, v204
	v_pk_mul_f32 v[176:177], v[178:179], v[160:161]
	v_mov_b32_e32 v158, v161
	v_mov_b32_e32 v135, v176
	v_mov_b32_e32 v175, v177
	v_pk_add_f32 v[176:177], v[134:135], v[174:175] neg_lo:[0,1] neg_hi:[0,1]
	v_pk_mul_f32 v[134:135], v[178:179], v[158:159]
	s_nop 0
	v_mov_b32_e32 v199, v134
	v_mov_b32_e32 v183, v135
	v_pk_add_f32 v[178:179], v[198:199], v[182:183]
	v_mov_b32_e32 v182, v132
	v_mov_b32_e32 v183, v133

; __device__ __forceinline__ f32x4 tof(const i32x4& a) { return (f32x4){(float)a.x, (float)a.y, (float)a.z, (float)a.w}; }
;     template <class AT> __device__ __forceinline__ void operator()(const AT (&acc)[2][2][4][2], const Unit& u, int wr, int wc, int fr, int fq) const {
;     ...
;         for (int ai = 0; ai < 2; ++ai)
; #pragma unroll
;             for (int m = 0; m < 4; ++m) { bf16_t* rowp = O + (size_t)(row0 + ai * HALF + m * 16) * INW + col0; const float rsc = sa[row0 + ai * HALF + m * 16] * sw;
;                 float cs[4], sn[4];
;                 if (dorope) { const int pos = (pt - 1) * 256 + wr * 64 + ai * HALF + m * 16 + fr; const float pp = (float)((wc >> 1) == 0 ? (pos >> 6) : (pos & 63));
; #pragma unroll
;                     for (int i = 0; i < 4; ++i) { const float ang = pp * inv[i]; cs[i] = __cosf(ang); sn[i] = __sinf(ang); } }
; #pragma unroll
;                 for (int bj = 0; bj < 2; ++bj) { f32x4 v0 = tof(acc[ai][bj][m][0]) * rsc, v1 = tof(acc[ai][bj][m][1]) * rsc;
;                     if (dorope) {
; #pragma unroll
;                         for (int i = 0; i < 4; ++i) { const float a = v0[i], b = v1[i]; v0[i] = a * cs[i] - b * sn[i]; v1[i] = b * cs[i] + a * sn[i]; } }
.LBB0_277:
	v_or_b32_e32 v170, 32, v152
	v_ashrrev_i32_e32 v171, 31, v170
	v_lshl_add_u64 v[132:133], v[170:171], 2, s[12:13]
	s_and_b64 vcc, exec, s[40:41]
	s_cbranch_vccnz .LBB0_279
	v_mov_b32_e32 v1, s30
	v_cndmask_b32_e64 v1, v188, v1, s[36:37]
	v_cvt_f32_i32_e32 v1, v1
	v_mul_f32_e32 v133, v191, v1
	v_mul_f32_e32 v133, 0.15915494, v133
	v_mul_f32_e32 v134, v192, v1
	v_cos_f32_e32 v156, v133
	v_sin_f32_e32 v154, v133
	v_mul_f32_e32 v133, v193, v1
	v_mul_f32_e32 v1, v194, v1
	v_mul_f32_e32 v134, 0.15915494, v134
	v_mul_f32_e32 v133, 0.15915494, v133
	v_mul_f32_e32 v1, 0.15915494, v1
	v_cos_f32_e32 v157, v134
	v_sin_f32_e32 v155, v134
	v_cos_f32_e32 v153, v133
	v_sin_f32_e32 v204, v133
	v_cos_f32_e32 v159, v1
	v_sin_f32_e32 v161, v1
.LBB0_279:
	v_cvt_f32_i32_e32 v135, v99
	v_cvt_f32_i32_e32 v134, v98
	v_mov_b32_e32 v132, v226
	v_mul_f32_e32 v172, v184, v132
	v_cvt_f32_i32_e32 v133, v97
	v_cvt_f32_i32_e32 v132, v96
	v_pk_mul_f32 v[176:177], v[172:173], v[134:135] op_sel_hi:[0,1]
	v_cvt_f32_i32_e32 v135, v95
	v_cvt_f32_i32_e32 v134, v94
	v_cvt_f32_i32_e32 v175, v93
	v_cvt_f32_i32_e32 v174, v92
	v_pk_mul_f32 v[182:183], v[172:173], v[132:133] op_sel_hi:[0,1]
	v_pk_mul_f32 v[178:179], v[172:173], v[134:135] op_sel_hi:[0,1]
	s_and_b64 vcc, exec, s[40:41]
	v_pk_mul_f32 v[180:181], v[172:173], v[174:175] op_sel_hi:[0,1]
	s_cbranch_vccnz .LBB0_281
	v_pk_mul_f32 v[132:133], v[180:181], v[154:155]
	v_pk_mul_f32 v[134:135], v[180:181], v[156:157]
	v_pk_fma_f32 v[132:133], v[182:183], v[156:157], v[132:133] neg_lo:[0,0,1] neg_hi:[0,0,1]
	v_pk_fma_f32 v[180:181], v[182:183], v[154:155], v[134:135]
	v_mul_f32_e32 v174, v178, v204
	v_mul_f32_e32 v182, v178, v153
	v_mov_b32_e32 v178, v177
	v_mov_b32_e32 v160, v159
	v_mul_f32_e32 v134, v176, v153
	v_mul_f32_e32 v198, v176, v204
	v_pk_mul_f32 v[176:177], v[178:179], v[160:161]
	v_mov_b32_e32 v158, v161
	v_mov_b32_e32 v135, v176
	v_mov_b32_e32 v175, v177
	v_pk_add_f32 v[176:177], v[134:135], v[174:175] neg_lo:[0,1] neg_hi:[0,1]
	v_pk_mul_f32 v[134:135], v[178:179], v[158:159]
	s_nop 0
	v_mov_b32_e32 v199, v134
	v_mov_b32_e32 v183, v135
	v_pk_add_f32 v[178:179], v[198:199], v[182:183]
	v_mov_b32_e32 v182, v132
	v_mov_b32_e32 v183, v133

; __device__ __forceinline__ f32x4 tof(const i32x4& a) { return (f32x4){(float)a.x, (float)a.y, (float)a.z, (float)a.w}; }
;     template <class AT> __device__ __forceinline__ void operator()(const AT (&acc)[2][2][4][2], const Unit& u, int wr, int wc, int fr, int fq) const {
;     ...
;         for (int ai = 0; ai < 2; ++ai)
; #pragma unroll
;             for (int m = 0; m < 4; ++m) { bf16_t* rowp = O + (size_t)(row0 + ai * HALF + m * 16) * INW + col0; const float rsc = sa[row0 + ai * HALF + m * 16] * sw;
;                 float cs[4], sn[4];
;                 if (dorope) { const int pos = (pt - 1) * 256 + wr * 64 + ai * HALF + m * 16 + fr; const float pp = (float)((wc >> 1) == 0 ? (pos >> 6) : (pos & 63));
; #pragma unroll
;                     for (int i = 0; i < 4; ++i) { const float ang = pp * inv[i]; cs[i] = __cosf(ang); sn[i] = __sinf(ang); } }
; #pragma unroll
;                 for (int bj = 0; bj < 2; ++bj) { f32x4 v0 = tof(acc[ai][bj][m][0]) * rsc, v1 = tof(acc[ai][bj][m][1]) * rsc;
;                     if (dorope) {
; #pragma unroll
;                         for (int i = 0; i < 4; ++i) { const float a = v0[i], b = v1[i]; v0[i] = a * cs[i] - b * sn[i]; v1[i] = b * cs[i] + a * sn[i]; } }
.LBB0_289:
	v_or_b32_e32 v170, 48, v152
	v_ashrrev_i32_e32 v171, 31, v170
	v_lshl_add_u64 v[132:133], v[170:171], 2, s[12:13]
	s_and_b64 vcc, exec, s[40:41]
	s_cbranch_vccnz .LBB0_291
	v_mov_b32_e32 v1, s30
	v_cndmask_b32_e64 v1, v189, v1, s[36:37]
	v_cvt_f32_i32_e32 v1, v1
	v_mul_f32_e32 v133, v191, v1
	v_mul_f32_e32 v133, 0.15915494, v133
	v_mul_f32_e32 v134, v192, v1
	v_cos_f32_e32 v156, v133
	v_sin_f32_e32 v154, v133
	v_mul_f32_e32 v133, v193, v1
	v_mul_f32_e32 v1, v194, v1
	v_mul_f32_e32 v134, 0.15915494, v134
	v_mul_f32_e32 v133, 0.15915494, v133
	v_mul_f32_e32 v1, 0.15915494, v1
	v_cos_f32_e32 v157, v134
	v_sin_f32_e32 v155, v134
	v_cos_f32_e32 v153, v133
	v_sin_f32_e32 v204, v133
	v_cos_f32_e32 v159, v1
	v_sin_f32_e32 v161, v1
.LBB0_291:
	v_cvt_f32_i32_e32 v135, v83
	v_cvt_f32_i32_e32 v134, v82
	v_mov_b32_e32 v132, v227
	v_mul_f32_e32 v172, v184, v132
	v_cvt_f32_i32_e32 v133, v81
	v_cvt_f32_i32_e32 v132, v80
	v_pk_mul_f32 v[176:177], v[172:173], v[134:135] op_sel_hi:[0,1]
	v_cvt_f32_i32_e32 v135, v79
	v_cvt_f32_i32_e32 v134, v78
	v_cvt_f32_i32_e32 v175, v77
	v_cvt_f32_i32_e32 v174, v76
	v_pk_mul_f32 v[182:183], v[172:173], v[132:133] op_sel_hi:[0,1]
	v_pk_mul_f32 v[178:179], v[172:173], v[134:135] op_sel_hi:[0,1]
	s_and_b64 vcc, exec, s[40:41]
	v_pk_mul_f32 v[180:181], v[172:173], v[174:175] op_sel_hi:[0,1]
	s_cbranch_vccnz .LBB0_293
	v_pk_mul_f32 v[132:133], v[180:181], v[154:155]
	v_pk_mul_f32 v[134:135], v[180:181], v[156:157]
	v_pk_fma_f32 v[132:133], v[182:183], v[156:157], v[132:133] neg_lo:[0,0,1] neg_hi:[0,0,1]
	v_pk_fma_f32 v[180:181], v[182:183], v[154:155], v[134:135]
	v_mul_f32_e32 v174, v178, v204
	v_mul_f32_e32 v182, v178, v153
	v_mov_b32_e32 v178, v177
	v_mov_b32_e32 v160, v159
	v_mul_f32_e32 v134, v176, v153
	v_mul_f32_e32 v198, v176, v204
	v_pk_mul_f32 v[176:177], v[178:179], v[160:161]
	v_mov_b32_e32 v158, v161
	v_mov_b32_e32 v135, v176
	v_mov_b32_e32 v175, v177
	v_pk_add_f32 v[176:177], v[134:135], v[174:175] neg_lo:[0,1] neg_hi:[0,1]
	v_pk_mul_f32 v[134:135], v[178:179], v[158:159]
	s_nop 0
	v_mov_b32_e32 v199, v134
	v_mov_b32_e32 v183, v135
	v_pk_add_f32 v[178:179], v[198:199], v[182:183]
	v_mov_b32_e32 v182, v132
	v_mov_b32_e32 v183, v133

; __device__ __forceinline__ f32x4 tof(const i32x4& a) { return (f32x4){(float)a.x, (float)a.y, (float)a.z, (float)a.w}; }
;     template <class AT> __device__ __forceinline__ void operator()(const AT (&acc)[2][2][4][2], const Unit& u, int wr, int wc, int fr, int fq) const {
;     ...
;         for (int ai = 0; ai < 2; ++ai)
; #pragma unroll
;             for (int m = 0; m < 4; ++m) { bf16_t* rowp = O + (size_t)(row0 + ai * HALF + m * 16) * INW + col0; const float rsc = sa[row0 + ai * HALF + m * 16] * sw;
;                 float cs[4], sn[4];
;                 if (dorope) { const int pos = (pt - 1) * 256 + wr * 64 + ai * HALF + m * 16 + fr; const float pp = (float)((wc >> 1) == 0 ? (pos >> 6) : (pos & 63));
; #pragma unroll
;                     for (int i = 0; i < 4; ++i) { const float ang = pp * inv[i]; cs[i] = __cosf(ang); sn[i] = __sinf(ang); } }
; #pragma unroll
;                 for (int bj = 0; bj < 2; ++bj) { f32x4 v0 = tof(acc[ai][bj][m][0]) * rsc, v1 = tof(acc[ai][bj][m][1]) * rsc;
;                     if (dorope) {
; #pragma unroll
;                         for (int i = 0; i < 4; ++i) { const float a = v0[i], b = v1[i]; v0[i] = a * cs[i] - b * sn[i]; v1[i] = b * cs[i] + a * sn[i]; } }
.LBB0_301:
	s_addk_i32 s25, 0x80
	s_and_b64 vcc, exec, s[40:41]
	s_ashr_i32 s25, s25, 6
	s_cbranch_vccnz .LBB0_303
	v_mov_b32_e32 v1, s25
	v_cndmask_b32_e64 v1, v185, v1, s[36:37]
	v_cvt_f32_i32_e32 v1, v1
	v_mul_f32_e32 v133, v191, v1
	v_mul_f32_e32 v133, 0.15915494, v133
	v_mul_f32_e32 v134, v192, v1
	v_cos_f32_e32 v156, v133
	v_sin_f32_e32 v154, v133
	v_mul_f32_e32 v133, v193, v1
	v_mul_f32_e32 v1, v194, v1
	v_mul_f32_e32 v134, 0.15915494, v134
	v_mul_f32_e32 v133, 0.15915494, v133
	v_mul_f32_e32 v1, 0.15915494, v1
	v_cos_f32_e32 v157, v134
	v_sin_f32_e32 v155, v134
	v_cos_f32_e32 v153, v133
	v_sin_f32_e32 v204, v133
	v_cos_f32_e32 v159, v1
	v_sin_f32_e32 v161, v1
.LBB0_303:
	v_cvt_f32_i32_e32 v135, v67
	v_cvt_f32_i32_e32 v134, v66
	v_mov_b32_e32 v132, v228
	v_mul_f32_e32 v170, v184, v132
	v_cvt_f32_i32_e32 v133, v65
	v_cvt_f32_i32_e32 v132, v64
	v_pk_mul_f32 v[174:175], v[170:171], v[134:135] op_sel_hi:[0,1]
	v_cvt_f32_i32_e32 v135, v63
	v_cvt_f32_i32_e32 v134, v62
	v_cvt_f32_i32_e32 v173, v61
	v_cvt_f32_i32_e32 v172, v60
	v_pk_mul_f32 v[180:181], v[170:171], v[132:133] op_sel_hi:[0,1]
	v_pk_mul_f32 v[176:177], v[170:171], v[134:135] op_sel_hi:[0,1]
	s_and_b64 vcc, exec, s[40:41]
	v_pk_mul_f32 v[178:179], v[170:171], v[172:173] op_sel_hi:[0,1]
	s_cbranch_vccnz .LBB0_305
	v_pk_mul_f32 v[132:133], v[178:179], v[154:155]
	v_pk_mul_f32 v[134:135], v[178:179], v[156:157]
	v_pk_fma_f32 v[132:133], v[180:181], v[156:157], v[132:133] neg_lo:[0,0,1] neg_hi:[0,0,1]
	v_pk_fma_f32 v[178:179], v[180:181], v[154:155], v[134:135]
	v_mul_f32_e32 v172, v176, v204
	v_mul_f32_e32 v180, v176, v153
	v_mov_b32_e32 v176, v175
	v_mov_b32_e32 v160, v159
	v_mul_f32_e32 v134, v174, v153
	v_mul_f32_e32 v182, v174, v204
	v_pk_mul_f32 v[174:175], v[176:177], v[160:161]
	v_mov_b32_e32 v158, v161
	v_mov_b32_e32 v135, v174
	v_mov_b32_e32 v173, v175
	v_pk_add_f32 v[174:175], v[134:135], v[172:173] neg_lo:[0,1] neg_hi:[0,1]
	v_pk_mul_f32 v[134:135], v[176:177], v[158:159]
	s_nop 0
	v_mov_b32_e32 v183, v134
	v_mov_b32_e32 v181, v135
	v_pk_add_f32 v[176:177], v[182:183], v[180:181]
	v_mov_b32_e32 v180, v132
	v_mov_b32_e32 v181, v133

; __device__ __forceinline__ f32x4 tof(const i32x4& a) { return (f32x4){(float)a.x, (float)a.y, (float)a.z, (float)a.w}; }
;     template <class AT> __device__ __forceinline__ void operator()(const AT (&acc)[2][2][4][2], const Unit& u, int wr, int wc, int fr, int fq) const {
;     ...
;         for (int ai = 0; ai < 2; ++ai)
; #pragma unroll
;             for (int m = 0; m < 4; ++m) { bf16_t* rowp = O + (size_t)(row0 + ai * HALF + m * 16) * INW + col0; const float rsc = sa[row0 + ai * HALF + m * 16] * sw;
;                 float cs[4], sn[4];
;                 if (dorope) { const int pos = (pt - 1) * 256 + wr * 64 + ai * HALF + m * 16 + fr; const float pp = (float)((wc >> 1) == 0 ? (pos >> 6) : (pos & 63));
; #pragma unroll
;                     for (int i = 0; i < 4; ++i) { const float ang = pp * inv[i]; cs[i] = __cosf(ang); sn[i] = __sinf(ang); } }
; #pragma unroll
;                 for (int bj = 0; bj < 2; ++bj) { f32x4 v0 = tof(acc[ai][bj][m][0]) * rsc, v1 = tof(acc[ai][bj][m][1]) * rsc;
;                     if (dorope) {
; #pragma unroll
;                         for (int i = 0; i < 4; ++i) { const float a = v0[i], b = v1[i]; v0[i] = a * cs[i] - b * sn[i]; v1[i] = b * cs[i] + a * sn[i]; } }
.LBB0_313:
	s_and_b64 vcc, exec, s[40:41]
	s_cbranch_vccnz .LBB0_315
	v_mov_b32_e32 v1, s25
	v_cndmask_b32_e64 v1, v187, v1, s[36:37]
	v_cvt_f32_i32_e32 v1, v1
	v_mul_f32_e32 v133, v191, v1
	v_mul_f32_e32 v133, 0.15915494, v133
	v_mul_f32_e32 v134, v192, v1
	v_cos_f32_e32 v156, v133
	v_sin_f32_e32 v154, v133
	v_mul_f32_e32 v133, v193, v1
	v_mul_f32_e32 v1, v194, v1
	v_mul_f32_e32 v134, 0.15915494, v134
	v_mul_f32_e32 v133, 0.15915494, v133
	v_mul_f32_e32 v1, 0.15915494, v1
	v_cos_f32_e32 v157, v134
	v_sin_f32_e32 v155, v134
	v_cos_f32_e32 v153, v133
	v_sin_f32_e32 v204, v133
	v_cos_f32_e32 v159, v1
	v_sin_f32_e32 v161, v1
.LBB0_315:
	v_cvt_f32_i32_e32 v135, v51
	v_cvt_f32_i32_e32 v134, v50
	v_mov_b32_e32 v132, v229
	v_mul_f32_e32 v170, v184, v132
	v_cvt_f32_i32_e32 v133, v49
	v_cvt_f32_i32_e32 v132, v48
	v_pk_mul_f32 v[174:175], v[170:171], v[134:135] op_sel_hi:[0,1]
	v_cvt_f32_i32_e32 v135, v47
	v_cvt_f32_i32_e32 v134, v46
	v_cvt_f32_i32_e32 v173, v45
	v_cvt_f32_i32_e32 v172, v44
	v_pk_mul_f32 v[180:181], v[170:171], v[132:133] op_sel_hi:[0,1]
	v_pk_mul_f32 v[176:177], v[170:171], v[134:135] op_sel_hi:[0,1]
	s_and_b64 vcc, exec, s[40:41]
	v_pk_mul_f32 v[178:179], v[170:171], v[172:173] op_sel_hi:[0,1]
	s_cbranch_vccnz .LBB0_317
	v_pk_mul_f32 v[132:133], v[178:179], v[154:155]
	v_pk_mul_f32 v[134:135], v[178:179], v[156:157]
	v_pk_fma_f32 v[132:133], v[180:181], v[156:157], v[132:133] neg_lo:[0,0,1] neg_hi:[0,0,1]
	v_pk_fma_f32 v[178:179], v[180:181], v[154:155], v[134:135]
	v_mul_f32_e32 v172, v176, v204
	v_mul_f32_e32 v180, v176, v153
	v_mov_b32_e32 v176, v175
	v_mov_b32_e32 v160, v159
	v_mul_f32_e32 v134, v174, v153
	v_mul_f32_e32 v182, v174, v204
	v_pk_mul_f32 v[174:175], v[176:177], v[160:161]
	v_mov_b32_e32 v158, v161
	v_mov_b32_e32 v135, v174
	v_mov_b32_e32 v173, v175
	v_pk_add_f32 v[174:175], v[134:135], v[172:173] neg_lo:[0,1] neg_hi:[0,1]
	v_pk_mul_f32 v[134:135], v[176:177], v[158:159]
	s_nop 0
	v_mov_b32_e32 v183, v134
	v_mov_b32_e32 v181, v135
	v_pk_add_f32 v[176:177], v[182:183], v[180:181]
	v_mov_b32_e32 v180, v132
	v_mov_b32_e32 v181, v133

; __device__ __forceinline__ f32x4 tof(const i32x4& a) { return (f32x4){(float)a.x, (float)a.y, (float)a.z, (float)a.w}; }
;     template <class AT> __device__ __forceinline__ void operator()(const AT (&acc)[2][2][4][2], const Unit& u, int wr, int wc, int fr, int fq) const {
;     ...
;         for (int ai = 0; ai < 2; ++ai)
; #pragma unroll
;             for (int m = 0; m < 4; ++m) { bf16_t* rowp = O + (size_t)(row0 + ai * HALF + m * 16) * INW + col0; const float rsc = sa[row0 + ai * HALF + m * 16] * sw;
;                 float cs[4], sn[4];
;                 if (dorope) { const int pos = (pt - 1) * 256 + wr * 64 + ai * HALF + m * 16 + fr; const float pp = (float)((wc >> 1) == 0 ? (pos >> 6) : (pos & 63));
; #pragma unroll
;                     for (int i = 0; i < 4; ++i) { const float ang = pp * inv[i]; cs[i] = __cosf(ang); sn[i] = __sinf(ang); } }
; #pragma unroll
;                 for (int bj = 0; bj < 2; ++bj) { f32x4 v0 = tof(acc[ai][bj][m][0]) * rsc, v1 = tof(acc[ai][bj][m][1]) * rsc;
;                     if (dorope) {
; #pragma unroll
;                         for (int i = 0; i < 4; ++i) { const float a = v0[i], b = v1[i]; v0[i] = a * cs[i] - b * sn[i]; v1[i] = b * cs[i] + a * sn[i]; } }
.LBB0_325:
	s_and_b64 vcc, exec, s[40:41]
	s_cbranch_vccnz .LBB0_327
	v_mov_b32_e32 v1, s25
	v_cndmask_b32_e64 v1, v188, v1, s[36:37]
	v_cvt_f32_i32_e32 v1, v1
	v_mul_f32_e32 v133, v191, v1
	v_mul_f32_e32 v133, 0.15915494, v133
	v_mul_f32_e32 v134, v192, v1
	v_cos_f32_e32 v156, v133
	v_sin_f32_e32 v154, v133
	v_mul_f32_e32 v133, v193, v1
	v_mul_f32_e32 v1, v194, v1
	v_mul_f32_e32 v134, 0.15915494, v134
	v_mul_f32_e32 v133, 0.15915494, v133
	v_mul_f32_e32 v1, 0.15915494, v1
	v_cos_f32_e32 v157, v134
	v_sin_f32_e32 v155, v134
	v_cos_f32_e32 v153, v133
	v_sin_f32_e32 v204, v133
	v_cos_f32_e32 v159, v1
	v_sin_f32_e32 v161, v1
.LBB0_327:
	v_cvt_f32_i32_e32 v135, v33
	v_cvt_f32_i32_e32 v134, v32
	v_mov_b32_e32 v132, v230
	v_mul_f32_e32 v170, v184, v132
	v_cvt_f32_i32_e32 v133, v31
	v_cvt_f32_i32_e32 v132, v30
	v_pk_mul_f32 v[174:175], v[170:171], v[134:135] op_sel_hi:[0,1]
	v_cvt_f32_i32_e32 v135, v29
	v_cvt_f32_i32_e32 v134, v28
	v_cvt_f32_i32_e32 v173, v27
	v_cvt_f32_i32_e32 v172, v26
	v_pk_mul_f32 v[180:181], v[170:171], v[132:133] op_sel_hi:[0,1]
	v_pk_mul_f32 v[176:177], v[170:171], v[134:135] op_sel_hi:[0,1]
	s_and_b64 vcc, exec, s[40:41]
	v_pk_mul_f32 v[178:179], v[170:171], v[172:173] op_sel_hi:[0,1]
	s_cbranch_vccnz .LBB0_329
	v_pk_mul_f32 v[132:133], v[178:179], v[154:155]
	v_pk_mul_f32 v[134:135], v[178:179], v[156:157]
	v_pk_fma_f32 v[132:133], v[180:181], v[156:157], v[132:133] neg_lo:[0,0,1] neg_hi:[0,0,1]
	v_pk_fma_f32 v[178:179], v[180:181], v[154:155], v[134:135]
	v_mul_f32_e32 v172, v176, v204
	v_mul_f32_e32 v180, v176, v153
	v_mov_b32_e32 v176, v175
	v_mov_b32_e32 v160, v159
	v_mul_f32_e32 v134, v174, v153
	v_mul_f32_e32 v182, v174, v204
	v_pk_mul_f32 v[174:175], v[176:177], v[160:161]
	v_mov_b32_e32 v158, v161
	v_mov_b32_e32 v135, v174
	v_mov_b32_e32 v173, v175
	v_pk_add_f32 v[174:175], v[134:135], v[172:173] neg_lo:[0,1] neg_hi:[0,1]
	v_pk_mul_f32 v[134:135], v[176:177], v[158:159]
	s_nop 0
	v_mov_b32_e32 v183, v134
	v_mov_b32_e32 v181, v135
	v_pk_add_f32 v[176:177], v[182:183], v[180:181]
	v_mov_b32_e32 v180, v132
	v_mov_b32_e32 v181, v133

; __device__ __forceinline__ f32x4 tof(const i32x4& a) { return (f32x4){(float)a.x, (float)a.y, (float)a.z, (float)a.w}; }
;     template <class AT> __device__ __forceinline__ void operator()(const AT (&acc)[2][2][4][2], const Unit& u, int wr, int wc, int fr, int fq) const {
;     ...
;         for (int ai = 0; ai < 2; ++ai)
; #pragma unroll
;             for (int m = 0; m < 4; ++m) { bf16_t* rowp = O + (size_t)(row0 + ai * HALF + m * 16) * INW + col0; const float rsc = sa[row0 + ai * HALF + m * 16] * sw;
;                 float cs[4], sn[4];
;                 if (dorope) { const int pos = (pt - 1) * 256 + wr * 64 + ai * HALF + m * 16 + fr; const float pp = (float)((wc >> 1) == 0 ? (pos >> 6) : (pos & 63));
; #pragma unroll
;                     for (int i = 0; i < 4; ++i) { const float ang = pp * inv[i]; cs[i] = __cosf(ang); sn[i] = __sinf(ang); } }
; #pragma unroll
;                 for (int bj = 0; bj < 2; ++bj) { f32x4 v0 = tof(acc[ai][bj][m][0]) * rsc, v1 = tof(acc[ai][bj][m][1]) * rsc;
;                     if (dorope) {
; #pragma unroll
;                         for (int i = 0; i < 4; ++i) { const float a = v0[i], b = v1[i]; v0[i] = a * cs[i] - b * sn[i]; v1[i] = b * cs[i] + a * sn[i]; } }
.LBB0_337:
	s_and_b64 vcc, exec, s[40:41]
	s_cbranch_vccnz .LBB0_339
	v_mov_b32_e32 v1, s25
	v_cndmask_b32_e64 v1, v189, v1, s[36:37]
	v_cvt_f32_i32_e32 v1, v1
	v_mul_f32_e32 v133, v191, v1
	v_mul_f32_e32 v133, 0.15915494, v133
	v_mul_f32_e32 v134, v192, v1
	v_cos_f32_e32 v156, v133
	v_sin_f32_e32 v154, v133
	v_mul_f32_e32 v133, v193, v1
	v_mul_f32_e32 v1, v194, v1
	v_mul_f32_e32 v134, 0.15915494, v134
	v_mul_f32_e32 v133, 0.15915494, v133
	v_mul_f32_e32 v1, 0.15915494, v1
	v_cos_f32_e32 v157, v134
	v_sin_f32_e32 v155, v134
	v_cos_f32_e32 v153, v133
	v_sin_f32_e32 v204, v133
	v_cos_f32_e32 v159, v1
	v_sin_f32_e32 v161, v1
.LBB0_339:
	v_cvt_f32_i32_e32 v135, v17
	v_cvt_f32_i32_e32 v134, v16
	v_mov_b32_e32 v132, v231
	v_mul_f32_e32 v162, v184, v132
	v_cvt_f32_i32_e32 v133, v15
	v_cvt_f32_i32_e32 v132, v14
	v_pk_mul_f32 v[170:171], v[162:163], v[134:135] op_sel_hi:[0,1]
	v_cvt_f32_i32_e32 v135, v13
	v_cvt_f32_i32_e32 v134, v12
	v_cvt_f32_i32_e32 v175, v11
	v_cvt_f32_i32_e32 v174, v10
	v_pk_mul_f32 v[176:177], v[162:163], v[132:133] op_sel_hi:[0,1]
	v_pk_mul_f32 v[172:173], v[162:163], v[134:135] op_sel_hi:[0,1]
	s_and_b64 vcc, exec, s[40:41]
	v_pk_mul_f32 v[174:175], v[162:163], v[174:175] op_sel_hi:[0,1]
	s_cbranch_vccnz .LBB0_341
	v_pk_mul_f32 v[132:133], v[174:175], v[154:155]
	v_pk_mul_f32 v[134:135], v[174:175], v[156:157]
	v_pk_fma_f32 v[132:133], v[176:177], v[156:157], v[132:133] neg_lo:[0,0,1] neg_hi:[0,0,1]
	v_pk_fma_f32 v[174:175], v[176:177], v[154:155], v[134:135]
	v_mul_f32_e32 v176, v172, v204
	v_mul_f32_e32 v178, v172, v153
	v_mov_b32_e32 v172, v171
	v_mov_b32_e32 v160, v159
	v_mul_f32_e32 v134, v170, v153
	v_mul_f32_e32 v180, v170, v204
	v_pk_mul_f32 v[170:171], v[172:173], v[160:161]
	v_mov_b32_e32 v158, v161
	v_mov_b32_e32 v135, v170
	v_mov_b32_e32 v177, v171
	v_pk_add_f32 v[170:171], v[134:135], v[176:177] neg_lo:[0,1] neg_hi:[0,1]
	v_pk_mul_f32 v[134:135], v[172:173], v[158:159]
	v_mov_b32_e32 v176, v132
	v_mov_b32_e32 v181, v134
	v_mov_b32_e32 v179, v135
	v_pk_add_f32 v[172:173], v[180:181], v[178:179]
	v_mov_b32_e32 v177, v133

; __device__ __forceinline__ f32x4 tof(const i32x4& a) { return (f32x4){(float)a.x, (float)a.y, (float)a.z, (float)a.w}; }
;     template <class AT> __device__ __forceinline__ void operator()(const AT (&acc)[2][2][4][2], const Unit& u, int wr, int wc, int fr, int fq) const {
;     ...
;         if (u.pn == 5 || (rope && u.pn >= 14)) {
;             const int b = u.pm / 17, qi = frl & 3, a4 = frl >> 2, nhv = u.pn == 5 ? 2 : 8, hv0 = u.pn == 5 ? 0 : (u.pn - 14) * 2; unsigned char* vq = u.pn == 5 ? v8a : v8b;
;             const unsigned sel = (unsigned)qi | ((unsigned)(4 + qi) << 8) | 0x0c0c0000u;
; #pragma unroll
;             for (int ai = 0; ai < 2; ++ai)
; #pragma unroll
;                 for (int m = 0; m < 4; ++m) { const float rsc = sa[row0 + ai * HALF + m * 16] * sw;
;                     const int tile = (u.pm % 17) * 4 + wr + 2 * ai, pos0 = 32 * (a4 & 1) + 16 * (m >> 1) + 4 * ((2 * m + (a4 >> 1)) & 3);
; #pragma unroll
;                     for (int bj = 0; bj < 2; ++bj) { const f32x4 v0 = tof(acc[ai][bj][m][0]) * rsc, v1 = tof(acc[ai][bj][m][1]) * rsc;
;                         unsigned char* tb_ = vq + ((size_t)((b * nhv + hv0 + bj) * 68 + tile)) * 8192 + (size_t)(wc * 32 + 8 * fql) * 64 + pos0;
; #pragma unroll
;                         for (int hh = 0; hh < 2; ++hh) { const f32x4 vv = hh ? v1 : v0; const int w = (int)pack_f8x4(vv[0], vv[1], vv[2], vv[3], 1.f);
;                             const unsigned p0 = (unsigned)__builtin_amdgcn_update_dpp(0, w, 0x00, 0xf, 0xf, false), p1 = (unsigned)__builtin_amdgcn_update_dpp(0, w, 0x55, 0xf, 0xf, false);
;                             const unsigned p2 = (unsigned)__builtin_amdgcn_update_dpp(0, w, 0xaa, 0xf, 0xf, false), p3 = (unsigned)__builtin_amdgcn_update_dpp(0, w, 0xff, 0xf, 0xf, false);
;                             const unsigned t01 = __builtin_amdgcn_perm(p1, p0, sel), t23 = __builtin_amdgcn_perm(p3, p2, sel);
;                             *(unsigned*)(tb_ + (hh * 4 + qi) * 64) = t01 | (t23 << 16); } } }
.LBB0_351:
	v_and_b32_e32 v1, 3, v203
	v_mul_u32_u24_e32 v132, 0x101, v1
	s_lshl_b32 s24, s24, 1
	v_or_b32_e32 v157, 0xc0c0400, v132
	v_lshlrev_b32_e32 v132, 3, v203
	s_sub_i32 s24, s24, 28
	v_and_b32_e32 v158, 32, v132
	v_lshrrev_b32_e32 v132, 1, v203
	s_and_b64 s[26:27], exec, s[26:27]
	v_and_b32_e32 v159, 12, v132
	v_lshl_add_u32 v132, v34, 3, s74
	s_cselect_b32 s24, 0, s24
	s_add_u32 s0, s4, s0
	v_ashrrev_i32_e32 v133, 31, v132
	v_ashrrev_i32_e32 v153, 31, v152
	s_addc_u32 s1, s5, s1
	v_lshlrev_b64 v[132:133], 6, v[132:133]
	v_lshl_add_u64 v[134:135], v[152:153], 2, s[12:13]
	v_lshl_add_u64 v[154:155], s[0:1], 0, v[132:133]
	v_lshlrev_b32_e32 v132, 6, v1
	global_load_dword v224, v[134:135], off
	global_load_dword v225, v[134:135], off offset:64
	global_load_dword v226, v[134:135], off offset:128
	global_load_dword v227, v[134:135], off offset:192
	global_load_dword v228, v[134:135], off offset:512
	global_load_dword v229, v[134:135], off offset:576
	global_load_dword v230, v[134:135], off offset:640
	global_load_dword v231, v[134:135], off offset:704
	v_cvt_f32_i32_e32 v129, v129
	v_cvt_f32_i32_e32 v128, v128
	v_cvt_f32_i32_e32 v131, v131
	v_cvt_f32_i32_e32 v130, v130
	s_lshl_b32 s17, s17, s25
	s_lshl_b32 s26, s19, 2
	s_add_i32 s17, s17, s24
	s_add_i32 s26, s26, s65
	s_mulk_i32 s17, 0x44
	v_cvt_f32_i32_e32 v161, v125
	v_cvt_f32_i32_e32 v160, v124
	s_add_i32 s0, s17, s26
	v_or_b32_e32 v34, v158, v159
	s_ashr_i32 s1, s0, 31
	v_lshl_add_u64 v[152:153], v[154:155], 0, v[34:35]
	s_lshl_b64 s[0:1], s[0:1], 13
	v_lshl_add_u64 v[124:125], v[152:153], 0, s[0:1]
	v_mov_b32_e32 v133, v35
	v_cvt_f32_i32_e32 v127, v127
	v_cvt_f32_i32_e32 v126, v126
	v_lshl_add_u64 v[124:125], v[124:125], 0, v[132:133]
	v_cvt_f32_i32_e32 v121, v121
	v_cvt_f32_i32_e32 v120, v120
	v_cvt_f32_i32_e32 v123, v123
	v_cvt_f32_i32_e32 v122, v122
	s_add_i32 s19, s17, 0x44
	v_cvt_f32_i32_e32 v117, v117
	v_cvt_f32_i32_e32 v116, v116
	s_add_i32 s24, s19, s26
	s_ashr_i32 s25, s24, 31
	s_lshl_b64 s[24:25], s[24:25], 13
	v_cvt_f32_i32_e32 v113, v113
	v_cvt_f32_i32_e32 v112, v112
	v_cvt_f32_i32_e32 v115, v115
	v_cvt_f32_i32_e32 v114, v114
	v_cvt_f32_i32_e32 v109, v109
	v_cvt_f32_i32_e32 v108, v108
	v_cvt_f32_i32_e32 v111, v111
	v_cvt_f32_i32_e32 v110, v110
	v_cvt_f32_i32_e32 v105, v105
	v_cvt_f32_i32_e32 v104, v104
	v_cvt_f32_i32_e32 v107, v107
	v_cvt_f32_i32_e32 v106, v106
	v_cvt_f32_i32_e32 v101, v101
	v_cvt_f32_i32_e32 v100, v100
	v_cvt_f32_i32_e32 v103, v103
	v_cvt_f32_i32_e32 v102, v102
	v_cvt_f32_i32_e32 v97, v97
	v_cvt_f32_i32_e32 v96, v96
	v_cvt_f32_i32_e32 v99, v99
	v_cvt_f32_i32_e32 v98, v98
	v_cvt_f32_i32_e32 v93, v93
	v_cvt_f32_i32_e32 v92, v92
	v_cvt_f32_i32_e32 v95, v95
	v_cvt_f32_i32_e32 v94, v94
	v_cvt_f32_i32_e32 v89, v89
	v_cvt_f32_i32_e32 v88, v88
	v_cvt_f32_i32_e32 v91, v91
	v_cvt_f32_i32_e32 v90, v90
	v_cvt_f32_i32_e32 v85, v85
	v_cvt_f32_i32_e32 v84, v84
	v_cvt_f32_i32_e32 v87, v87
	v_cvt_f32_i32_e32 v86, v86
	v_cvt_f32_i32_e32 v81, v81
	v_cvt_f32_i32_e32 v80, v80
	v_xor_b32_e32 v34, 8, v34
	v_cvt_f32_i32_e32 v83, v83
	v_cvt_f32_i32_e32 v82, v82
	v_cvt_f32_i32_e32 v77, v77
	v_cvt_f32_i32_e32 v76, v76
	v_cvt_f32_i32_e32 v79, v79
	v_cvt_f32_i32_e32 v78, v78
	v_cvt_f32_i32_e32 v73, v73
	v_cvt_f32_i32_e32 v72, v72
	v_cvt_f32_i32_e32 v75, v75
	v_cvt_f32_i32_e32 v74, v74
	v_cvt_f32_i32_e32 v69, v69
	v_cvt_f32_i32_e32 v68, v68
	v_cvt_f32_i32_e32 v71, v71
	s_waitcnt vmcnt(0)
	v_mov_b32_e32 v1, v224
	v_mul_f32_e32 v156, v184, v1
	v_pk_mul_f32 v[128:129], v[156:157], v[128:129] op_sel_hi:[0,1]
	v_med3_f32 v1, v128, s33, v217
	v_med3_f32 v128, v129, s33, v217
	v_mov_b32_e32 v129, v35
	v_cvt_pk_fp8_f32 v129, v1, v128
	v_pk_mul_f32 v[130:131], v[156:157], v[130:131] op_sel_hi:[0,1]
	v_med3_f32 v1, v130, s33, v217
	v_med3_f32 v128, v131, s33, v217
	v_cvt_pk_fp8_f32 v129, v1, v128 op_sel:[0,0,1]
	v_mov_b32_e32 v1, v35
	v_mov_b32_e32 v128, v35
	v_mov_b32_e32 v130, v35
	v_mov_b32_e32 v131, v35
	v_mov_b32_dpp v1, v129 quad_perm:[0,0,0,0] row_mask:0xf bank_mask:0xf
	v_mov_b32_dpp v128, v129 quad_perm:[1,1,1,1] row_mask:0xf bank_mask:0xf
	v_mov_b32_dpp v130, v129 quad_perm:[2,2,2,2] row_mask:0xf bank_mask:0xf
	v_mov_b32_dpp v131, v129 quad_perm:[3,3,3,3] row_mask:0xf bank_mask:0xf
	v_perm_b32 v1, v128, v1, v157
	v_perm_b32 v128, v131, v130, v157
	v_lshl_or_b32 v1, v128, 16, v1
	v_pk_mul_f32 v[128:129], v[156:157], v[160:161] op_sel_hi:[0,1]
	global_store_dword v[124:125], v1, off
	v_med3_f32 v1, v128, s33, v217
	v_med3_f32 v128, v129, s33, v217
	v_mov_b32_e32 v129, v35
	v_cvt_pk_fp8_f32 v129, v1, v128
	v_pk_mul_f32 v[126:127], v[156:157], v[126:127] op_sel_hi:[0,1]
	v_med3_f32 v1, v126, s33, v217
	v_med3_f32 v126, v127, s33, v217
	v_cvt_pk_fp8_f32 v129, v1, v126 op_sel:[0,0,1]
	v_mov_b32_e32 v1, v35
	v_mov_b32_e32 v126, v35
	v_mov_b32_e32 v127, v35
	v_mov_b32_e32 v128, v35
	v_mov_b32_dpp v1, v129 quad_perm:[0,0,0,0] row_mask:0xf bank_mask:0xf
	v_mov_b32_dpp v126, v129 quad_perm:[1,1,1,1] row_mask:0xf bank_mask:0xf
	v_mov_b32_dpp v127, v129 quad_perm:[2,2,2,2] row_mask:0xf bank_mask:0xf
	v_mov_b32_dpp v128, v129 quad_perm:[3,3,3,3] row_mask:0xf bank_mask:0xf
	v_perm_b32 v1, v126, v1, v157
	v_perm_b32 v126, v128, v127, v157
	v_lshl_or_b32 v1, v126, 16, v1
	v_pk_mul_f32 v[120:121], v[156:157], v[120:121] op_sel_hi:[0,1]
	global_store_dword v[124:125], v1, off offset:256
	v_med3_f32 v1, v120, s33, v217
	v_med3_f32 v120, v121, s33, v217
	v_mov_b32_e32 v121, v35
	v_cvt_pk_fp8_f32 v121, v1, v120
	v_pk_mul_f32 v[122:123], v[156:157], v[122:123] op_sel_hi:[0,1]
	v_med3_f32 v1, v122, s33, v217
	v_med3_f32 v120, v123, s33, v217
	v_cvt_pk_fp8_f32 v121, v1, v120 op_sel:[0,0,1]
; __device__ __forceinline__ f32x4 tof(const i32x4& a) { return (f32x4){(float)a.x, (float)a.y, (float)a.z, (float)a.w}; }
;     template <class AT> __device__ __forceinline__ void operator()(const AT (&acc)[2][2][4][2], const Unit& u, int wr, int wc, int fr, int fq) const {
;     ...
;             for (int ai = 0; ai < 2; ++ai)
; #pragma unroll
;                 for (int m = 0; m < 4; ++m) { const float rsc = sa[row0 + ai * HALF + m * 16] * sw;
;                     const int tile = (u.pm % 17) * 4 + wr + 2 * ai, pos0 = 32 * (a4 & 1) + 16 * (m >> 1) + 4 * ((2 * m + (a4 >> 1)) & 3);
; #pragma unroll
;                     for (int bj = 0; bj < 2; ++bj) { const f32x4 v0 = tof(acc[ai][bj][m][0]) * rsc, v1 = tof(acc[ai][bj][m][1]) * rsc;
;                         unsigned char* tb_ = vq + ((size_t)((b * nhv + hv0 + bj) * 68 + tile)) * 8192 + (size_t)(wc * 32 + 8 * fql) * 64 + pos0;
; #pragma unroll
;                         for (int hh = 0; hh < 2; ++hh) { const f32x4 vv = hh ? v1 : v0; const int w = (int)pack_f8x4(vv[0], vv[1], vv[2], vv[3], 1.f);
;                             const unsigned p0 = (unsigned)__builtin_amdgcn_update_dpp(0, w, 0x00, 0xf, 0xf, false), p1 = (unsigned)__builtin_amdgcn_update_dpp(0, w, 0x55, 0xf, 0xf, false);
;                             const unsigned p2 = (unsigned)__builtin_amdgcn_update_dpp(0, w, 0xaa, 0xf, 0xf, false), p3 = (unsigned)__builtin_amdgcn_update_dpp(0, w, 0xff, 0xf, 0xf, false);
;                             const unsigned t01 = __builtin_amdgcn_perm(p1, p0, sel), t23 = __builtin_amdgcn_perm(p3, p2, sel);
;                             *(unsigned*)(tb_ + (hh * 4 + qi) * 64) = t01 | (t23 << 16); } } }
	v_mov_b32_e32 v1, v35
	v_mov_b32_e32 v120, v35
	v_mov_b32_e32 v122, v35
	v_mov_b32_e32 v123, v35
	v_mov_b32_dpp v1, v121 quad_perm:[0,0,0,0] row_mask:0xf bank_mask:0xf
	v_mov_b32_dpp v120, v121 quad_perm:[1,1,1,1] row_mask:0xf bank_mask:0xf
	v_mov_b32_dpp v122, v121 quad_perm:[2,2,2,2] row_mask:0xf bank_mask:0xf
	v_mov_b32_dpp v123, v121 quad_perm:[3,3,3,3] row_mask:0xf bank_mask:0xf
	v_cvt_f32_i32_e32 v127, v119
	v_cvt_f32_i32_e32 v126, v118
	v_lshl_add_u64 v[118:119], v[152:153], 0, s[24:25]
	v_perm_b32 v1, v120, v1, v157
	v_perm_b32 v120, v123, v122, v157
	v_lshl_or_b32 v1, v120, 16, v1
	v_lshl_add_u64 v[118:119], v[118:119], 0, v[132:133]
	v_pk_mul_f32 v[116:117], v[156:157], v[116:117] op_sel_hi:[0,1]
	global_store_dword v[118:119], v1, off
	v_med3_f32 v1, v116, s33, v217
	v_med3_f32 v116, v117, s33, v217
	v_mov_b32_e32 v117, v35
	v_cvt_pk_fp8_f32 v117, v1, v116
	v_pk_mul_f32 v[120:121], v[156:157], v[126:127] op_sel_hi:[0,1]
	v_med3_f32 v1, v120, s33, v217
	v_med3_f32 v116, v121, s33, v217
	v_cvt_pk_fp8_f32 v117, v1, v116 op_sel:[0,0,1]
	v_mov_b32_e32 v1, v35
	v_mov_b32_e32 v116, v35
	v_mov_b32_e32 v120, v35
	v_mov_b32_e32 v121, v35
	v_mov_b32_dpp v1, v117 quad_perm:[0,0,0,0] row_mask:0xf bank_mask:0xf
	v_mov_b32_dpp v116, v117 quad_perm:[1,1,1,1] row_mask:0xf bank_mask:0xf
	v_mov_b32_dpp v120, v117 quad_perm:[2,2,2,2] row_mask:0xf bank_mask:0xf
	v_mov_b32_dpp v121, v117 quad_perm:[3,3,3,3] row_mask:0xf bank_mask:0xf
	v_perm_b32 v1, v116, v1, v157
	v_perm_b32 v116, v121, v120, v157
	v_lshl_or_b32 v1, v116, 16, v1
	global_store_dword v[118:119], v1, off offset:256
	v_bitop3_b32 v116, v158, 8, v159 bitop3:0x36
	v_mov_b32_e32 v117, v35
	v_lshl_add_u64 v[116:117], v[154:155], 0, v[116:117]
	v_lshl_add_u64 v[122:123], v[116:117], 0, s[0:1]
	v_cvt_f32_i32_e32 v70, v70
	v_cvt_f32_i32_e32 v65, v65
	v_cvt_f32_i32_e32 v64, v64
	v_cvt_f32_i32_e32 v67, v67
	v_cvt_f32_i32_e32 v66, v66
	s_add_i32 s26, s26, 2
	v_cvt_f32_i32_e32 v63, v63
	v_cvt_f32_i32_e32 v62, v62
	v_cvt_f32_i32_e32 v57, v57
	v_cvt_f32_i32_e32 v56, v56
	v_cvt_f32_i32_e32 v59, v59
	v_cvt_f32_i32_e32 v58, v58
	v_cvt_f32_i32_e32 v55, v55
	v_cvt_f32_i32_e32 v54, v54
	v_cvt_f32_i32_e32 v49, v49
	v_cvt_f32_i32_e32 v48, v48
	v_cvt_f32_i32_e32 v51, v51
	v_cvt_f32_i32_e32 v50, v50
	v_cvt_f32_i32_e32 v45, v45
	v_cvt_f32_i32_e32 v44, v44
	v_cvt_f32_i32_e32 v47, v47
	v_cvt_f32_i32_e32 v46, v46
	v_cvt_f32_i32_e32 v41, v41
	v_cvt_f32_i32_e32 v40, v40
	v_cvt_f32_i32_e32 v43, v43
	v_cvt_f32_i32_e32 v42, v42
	v_cvt_f32_i32_e32 v37, v37
	v_cvt_f32_i32_e32 v36, v36
	v_cvt_f32_i32_e32 v39, v39
	v_cvt_f32_i32_e32 v38, v38
	v_cvt_f32_i32_e32 v31, v31
	v_cvt_f32_i32_e32 v30, v30
	v_cvt_f32_i32_e32 v33, v33
	v_cvt_f32_i32_e32 v32, v32
	v_cvt_f32_i32_e32 v27, v27
	v_cvt_f32_i32_e32 v26, v26
	v_cvt_f32_i32_e32 v29, v29
	v_cvt_f32_i32_e32 v28, v28
	v_cvt_f32_i32_e32 v23, v23
	v_cvt_f32_i32_e32 v22, v22
	v_cvt_f32_i32_e32 v25, v25
	v_cvt_f32_i32_e32 v24, v24
	v_cvt_f32_i32_e32 v19, v19
	v_cvt_f32_i32_e32 v18, v18
	v_cvt_f32_i32_e32 v21, v21
	v_cvt_f32_i32_e32 v20, v20
	v_cvt_f32_i32_e32 v15, v15
	v_cvt_f32_i32_e32 v14, v14
	v_cvt_f32_i32_e32 v17, v17
	v_cvt_f32_i32_e32 v16, v16
	v_cvt_f32_i32_e32 v11, v11
	v_cvt_f32_i32_e32 v10, v10
	v_cvt_f32_i32_e32 v13, v13
	v_cvt_f32_i32_e32 v12, v12
	v_cvt_f32_i32_e32 v7, v7
	v_cvt_f32_i32_e32 v6, v6
	v_cvt_f32_i32_e32 v9, v9
	v_cvt_f32_i32_e32 v8, v8
	v_cvt_f32_i32_e32 v3, v3
	v_cvt_f32_i32_e32 v2, v2
	v_cvt_f32_i32_e32 v5, v5
	v_cvt_f32_i32_e32 v4, v4
	v_mov_b32_e32 v1, v225
	v_mul_f32_e32 v120, v184, v1
	v_pk_mul_f32 v[112:113], v[120:121], v[112:113] op_sel_hi:[0,1]
	v_med3_f32 v1, v112, s33, v217
	v_med3_f32 v112, v113, s33, v217
	v_mov_b32_e32 v113, v35
	v_cvt_pk_fp8_f32 v113, v1, v112
	v_pk_mul_f32 v[114:115], v[120:121], v[114:115] op_sel_hi:[0,1]
	v_med3_f32 v1, v114, s33, v217
	v_med3_f32 v112, v115, s33, v217
	v_cvt_pk_fp8_f32 v113, v1, v112 op_sel:[0,0,1]
	v_mov_b32_e32 v1, v35
	v_mov_b32_e32 v112, v35
	v_mov_b32_e32 v114, v35
	v_mov_b32_e32 v115, v35
	v_mov_b32_dpp v1, v113 quad_perm:[0,0,0,0] row_mask:0xf bank_mask:0xf
	v_mov_b32_dpp v112, v113 quad_perm:[1,1,1,1] row_mask:0xf bank_mask:0xf
	v_mov_b32_dpp v114, v113 quad_perm:[2,2,2,2] row_mask:0xf bank_mask:0xf
	v_mov_b32_dpp v115, v113 quad_perm:[3,3,3,3] row_mask:0xf bank_mask:0xf
	v_perm_b32 v1, v112, v1, v157
	v_perm_b32 v112, v115, v114, v157
	v_lshl_or_b32 v1, v112, 16, v1
	v_lshl_add_u64 v[112:113], v[122:123], 0, v[132:133]
	v_pk_mul_f32 v[108:109], v[120:121], v[108:109] op_sel_hi:[0,1]
	global_store_dword v[112:113], v1, off
	v_med3_f32 v1, v108, s33, v217
	v_med3_f32 v108, v109, s33, v217
	v_mov_b32_e32 v109, v35
	v_cvt_pk_fp8_f32 v109, v1, v108
	v_pk_mul_f32 v[110:111], v[120:121], v[110:111] op_sel_hi:[0,1]
	v_med3_f32 v1, v110, s33, v217
	v_med3_f32 v108, v111, s33, v217
	v_cvt_pk_fp8_f32 v109, v1, v108 op_sel:[0,0,1]
	v_mov_b32_e32 v1, v35
	v_mov_b32_e32 v108, v35
	v_mov_b32_e32 v110, v35
	v_mov_b32_e32 v111, v35
	v_mov_b32_dpp v1, v109 quad_perm:[0,0,0,0] row_mask:0xf bank_mask:0xf
	v_mov_b32_dpp v108, v109 quad_perm:[1,1,1,1] row_mask:0xf bank_mask:0xf
	v_mov_b32_dpp v110, v109 quad_perm:[2,2,2,2] row_mask:0xf bank_mask:0xf
	v_mov_b32_dpp v111, v109 quad_perm:[3,3,3,3] row_mask:0xf bank_mask:0xf
	v_perm_b32 v1, v108, v1, v157
	v_perm_b32 v108, v111, v110, v157
	v_lshl_or_b32 v1, v108, 16, v1
	v_pk_mul_f32 v[104:105], v[120:121], v[104:105] op_sel_hi:[0,1]
	global_store_dword v[112:113], v1, off offset:256
	v_med3_f32 v1, v104, s33, v217
	v_med3_f32 v104, v105, s33, v217
	v_mov_b32_e32 v105, v35
	v_cvt_pk_fp8_f32 v105, v1, v104
	v_pk_mul_f32 v[106:107], v[120:121], v[106:107] op_sel_hi:[0,1]
; __device__ __forceinline__ f32x4 tof(const i32x4& a) { return (f32x4){(float)a.x, (float)a.y, (float)a.z, (float)a.w}; }
;     template <class AT> __device__ __forceinline__ void operator()(const AT (&acc)[2][2][4][2], const Unit& u, int wr, int wc, int fr, int fq) const {
;     ...
;             for (int ai = 0; ai < 2; ++ai)
; #pragma unroll
;                 for (int m = 0; m < 4; ++m) { const float rsc = sa[row0 + ai * HALF + m * 16] * sw;
;                     const int tile = (u.pm % 17) * 4 + wr + 2 * ai, pos0 = 32 * (a4 & 1) + 16 * (m >> 1) + 4 * ((2 * m + (a4 >> 1)) & 3);
; #pragma unroll
;                     for (int bj = 0; bj < 2; ++bj) { const f32x4 v0 = tof(acc[ai][bj][m][0]) * rsc, v1 = tof(acc[ai][bj][m][1]) * rsc;
;                         unsigned char* tb_ = vq + ((size_t)((b * nhv + hv0 + bj) * 68 + tile)) * 8192 + (size_t)(wc * 32 + 8 * fql) * 64 + pos0;
; #pragma unroll
;                         for (int hh = 0; hh < 2; ++hh) { const f32x4 vv = hh ? v1 : v0; const int w = (int)pack_f8x4(vv[0], vv[1], vv[2], vv[3], 1.f);
;                             const unsigned p0 = (unsigned)__builtin_amdgcn_update_dpp(0, w, 0x00, 0xf, 0xf, false), p1 = (unsigned)__builtin_amdgcn_update_dpp(0, w, 0x55, 0xf, 0xf, false);
;                             const unsigned p2 = (unsigned)__builtin_amdgcn_update_dpp(0, w, 0xaa, 0xf, 0xf, false), p3 = (unsigned)__builtin_amdgcn_update_dpp(0, w, 0xff, 0xf, 0xf, false);
;                             const unsigned t01 = __builtin_amdgcn_perm(p1, p0, sel), t23 = __builtin_amdgcn_perm(p3, p2, sel);
;                             *(unsigned*)(tb_ + (hh * 4 + qi) * 64) = t01 | (t23 << 16); } } }
	v_med3_f32 v1, v106, s33, v217
	v_med3_f32 v104, v107, s33, v217
	v_cvt_pk_fp8_f32 v105, v1, v104 op_sel:[0,0,1]
	v_mov_b32_e32 v1, v35
	v_mov_b32_e32 v104, v35
	v_mov_b32_e32 v106, v35
	v_mov_b32_e32 v107, v35
	v_mov_b32_dpp v1, v105 quad_perm:[0,0,0,0] row_mask:0xf bank_mask:0xf
	v_mov_b32_dpp v104, v105 quad_perm:[1,1,1,1] row_mask:0xf bank_mask:0xf
	v_mov_b32_dpp v106, v105 quad_perm:[2,2,2,2] row_mask:0xf bank_mask:0xf
	v_mov_b32_dpp v107, v105 quad_perm:[3,3,3,3] row_mask:0xf bank_mask:0xf
	v_lshl_add_u64 v[108:109], v[116:117], 0, s[24:25]
	v_perm_b32 v1, v104, v1, v157
	v_perm_b32 v104, v107, v106, v157
	v_lshl_or_b32 v1, v104, 16, v1
	v_lshl_add_u64 v[104:105], v[108:109], 0, v[132:133]
	v_pk_mul_f32 v[100:101], v[120:121], v[100:101] op_sel_hi:[0,1]
	global_store_dword v[104:105], v1, off
	v_med3_f32 v1, v100, s33, v217
	v_med3_f32 v100, v101, s33, v217
	v_mov_b32_e32 v101, v35
	v_cvt_pk_fp8_f32 v101, v1, v100
	v_pk_mul_f32 v[102:103], v[120:121], v[102:103] op_sel_hi:[0,1]
	v_med3_f32 v1, v102, s33, v217
	v_med3_f32 v100, v103, s33, v217
	v_cvt_pk_fp8_f32 v101, v1, v100 op_sel:[0,0,1]
	v_mov_b32_e32 v1, v35
	v_mov_b32_e32 v100, v35
	v_mov_b32_e32 v102, v35
	v_mov_b32_e32 v103, v35
	v_mov_b32_dpp v1, v101 quad_perm:[0,0,0,0] row_mask:0xf bank_mask:0xf
	v_mov_b32_dpp v100, v101 quad_perm:[1,1,1,1] row_mask:0xf bank_mask:0xf
	v_mov_b32_dpp v102, v101 quad_perm:[2,2,2,2] row_mask:0xf bank_mask:0xf
	v_mov_b32_dpp v103, v101 quad_perm:[3,3,3,3] row_mask:0xf bank_mask:0xf
	v_perm_b32 v1, v100, v1, v157
	v_perm_b32 v100, v103, v102, v157
	v_lshl_or_b32 v1, v100, 16, v1
	global_store_dword v[104:105], v1, off offset:256
	v_mov_b32_e32 v1, v226
	v_mul_f32_e32 v100, v184, v1
	v_pk_mul_f32 v[96:97], v[100:101], v[96:97] op_sel_hi:[0,1]
	v_med3_f32 v1, v96, s33, v217
	v_med3_f32 v96, v97, s33, v217
	v_mov_b32_e32 v97, v35
	v_cvt_pk_fp8_f32 v97, v1, v96
	v_pk_mul_f32 v[98:99], v[100:101], v[98:99] op_sel_hi:[0,1]
	v_med3_f32 v1, v98, s33, v217
	v_med3_f32 v96, v99, s33, v217
	v_cvt_pk_fp8_f32 v97, v1, v96 op_sel:[0,0,1]
	v_mov_b32_e32 v1, v35
	v_mov_b32_e32 v96, v35
	v_mov_b32_e32 v98, v35
	v_mov_b32_e32 v99, v35
	v_mov_b32_dpp v1, v97 quad_perm:[0,0,0,0] row_mask:0xf bank_mask:0xf
	v_mov_b32_dpp v96, v97 quad_perm:[1,1,1,1] row_mask:0xf bank_mask:0xf
	v_mov_b32_dpp v98, v97 quad_perm:[2,2,2,2] row_mask:0xf bank_mask:0xf
	v_mov_b32_dpp v99, v97 quad_perm:[3,3,3,3] row_mask:0xf bank_mask:0xf
	v_perm_b32 v1, v96, v1, v157
	v_perm_b32 v96, v99, v98, v157
	v_lshl_or_b32 v1, v96, 16, v1
	v_pk_mul_f32 v[92:93], v[100:101], v[92:93] op_sel_hi:[0,1]
	global_store_dword v[124:125], v1, off offset:16
	v_med3_f32 v1, v92, s33, v217
	v_med3_f32 v92, v93, s33, v217
	v_mov_b32_e32 v93, v35
	v_cvt_pk_fp8_f32 v93, v1, v92
	v_pk_mul_f32 v[94:95], v[100:101], v[94:95] op_sel_hi:[0,1]
	v_med3_f32 v1, v94, s33, v217
	v_med3_f32 v92, v95, s33, v217
	v_cvt_pk_fp8_f32 v93, v1, v92 op_sel:[0,0,1]
	v_mov_b32_e32 v1, v35
	v_mov_b32_e32 v92, v35
	v_mov_b32_e32 v94, v35
	v_mov_b32_e32 v95, v35
	v_mov_b32_dpp v1, v93 quad_perm:[0,0,0,0] row_mask:0xf bank_mask:0xf
	v_mov_b32_dpp v92, v93 quad_perm:[1,1,1,1] row_mask:0xf bank_mask:0xf
	v_mov_b32_dpp v94, v93 quad_perm:[2,2,2,2] row_mask:0xf bank_mask:0xf
	v_mov_b32_dpp v95, v93 quad_perm:[3,3,3,3] row_mask:0xf bank_mask:0xf
	v_perm_b32 v1, v92, v1, v157
	v_perm_b32 v92, v95, v94, v157
	v_lshl_or_b32 v1, v92, 16, v1
	v_pk_mul_f32 v[88:89], v[100:101], v[88:89] op_sel_hi:[0,1]
	global_store_dword v[124:125], v1, off offset:272
	v_med3_f32 v1, v88, s33, v217
	v_med3_f32 v88, v89, s33, v217
	v_mov_b32_e32 v89, v35
	v_cvt_pk_fp8_f32 v89, v1, v88
	v_pk_mul_f32 v[90:91], v[100:101], v[90:91] op_sel_hi:[0,1]
	v_med3_f32 v1, v90, s33, v217
	v_med3_f32 v88, v91, s33, v217
	v_cvt_pk_fp8_f32 v89, v1, v88 op_sel:[0,0,1]
	v_mov_b32_e32 v1, v35
	v_mov_b32_e32 v88, v35
	v_mov_b32_e32 v90, v35
	v_mov_b32_e32 v91, v35
	v_mov_b32_dpp v1, v89 quad_perm:[0,0,0,0] row_mask:0xf bank_mask:0xf
	v_mov_b32_dpp v88, v89 quad_perm:[1,1,1,1] row_mask:0xf bank_mask:0xf
	v_mov_b32_dpp v90, v89 quad_perm:[2,2,2,2] row_mask:0xf bank_mask:0xf
	v_mov_b32_dpp v91, v89 quad_perm:[3,3,3,3] row_mask:0xf bank_mask:0xf
	v_perm_b32 v1, v88, v1, v157
	v_perm_b32 v88, v91, v90, v157
	v_lshl_or_b32 v1, v88, 16, v1
	v_pk_mul_f32 v[84:85], v[100:101], v[84:85] op_sel_hi:[0,1]
	global_store_dword v[118:119], v1, off offset:16
	v_med3_f32 v1, v84, s33, v217
	v_med3_f32 v84, v85, s33, v217
	v_mov_b32_e32 v85, v35
	v_cvt_pk_fp8_f32 v85, v1, v84
	v_pk_mul_f32 v[86:87], v[100:101], v[86:87] op_sel_hi:[0,1]
	v_med3_f32 v1, v86, s33, v217
	v_med3_f32 v84, v87, s33, v217
	v_cvt_pk_fp8_f32 v85, v1, v84 op_sel:[0,0,1]
	v_mov_b32_e32 v1, v35
	v_mov_b32_e32 v84, v35
	v_mov_b32_e32 v86, v35
	v_mov_b32_e32 v87, v35
	v_mov_b32_dpp v1, v85 quad_perm:[0,0,0,0] row_mask:0xf bank_mask:0xf
	v_mov_b32_dpp v84, v85 quad_perm:[1,1,1,1] row_mask:0xf bank_mask:0xf
	v_mov_b32_dpp v86, v85 quad_perm:[2,2,2,2] row_mask:0xf bank_mask:0xf
	v_mov_b32_dpp v87, v85 quad_perm:[3,3,3,3] row_mask:0xf bank_mask:0xf
	v_perm_b32 v1, v84, v1, v157
	v_perm_b32 v84, v87, v86, v157
	v_lshl_or_b32 v1, v84, 16, v1
	global_store_dword v[118:119], v1, off offset:272
	v_lshl_add_u64 v[84:85], v[154:155], 0, v[34:35]
	v_lshl_add_u64 v[88:89], v[84:85], 0, s[0:1]
	s_add_i32 s0, s17, s26
	s_ashr_i32 s1, s0, 31
	v_mov_b32_e32 v1, v227
	v_mul_f32_e32 v86, v184, v1
	v_pk_mul_f32 v[80:81], v[86:87], v[80:81] op_sel_hi:[0,1]
	v_med3_f32 v1, v80, s33, v217
	v_med3_f32 v34, v81, s33, v217
	v_mov_b32_e32 v80, v35
	v_cvt_pk_fp8_f32 v80, v1, v34
	v_pk_mul_f32 v[82:83], v[86:87], v[82:83] op_sel_hi:[0,1]
	v_med3_f32 v1, v82, s33, v217
; __device__ __forceinline__ f32x4 tof(const i32x4& a) { return (f32x4){(float)a.x, (float)a.y, (float)a.z, (float)a.w}; }
;     template <class AT> __device__ __forceinline__ void operator()(const AT (&acc)[2][2][4][2], const Unit& u, int wr, int wc, int fr, int fq) const {
;     ...
;             for (int ai = 0; ai < 2; ++ai)
; #pragma unroll
;                 for (int m = 0; m < 4; ++m) { const float rsc = sa[row0 + ai * HALF + m * 16] * sw;
;                     const int tile = (u.pm % 17) * 4 + wr + 2 * ai, pos0 = 32 * (a4 & 1) + 16 * (m >> 1) + 4 * ((2 * m + (a4 >> 1)) & 3);
; #pragma unroll
;                     for (int bj = 0; bj < 2; ++bj) { const f32x4 v0 = tof(acc[ai][bj][m][0]) * rsc, v1 = tof(acc[ai][bj][m][1]) * rsc;
;                         unsigned char* tb_ = vq + ((size_t)((b * nhv + hv0 + bj) * 68 + tile)) * 8192 + (size_t)(wc * 32 + 8 * fql) * 64 + pos0;
; #pragma unroll
;                         for (int hh = 0; hh < 2; ++hh) { const f32x4 vv = hh ? v1 : v0; const int w = (int)pack_f8x4(vv[0], vv[1], vv[2], vv[3], 1.f);
;                             const unsigned p0 = (unsigned)__builtin_amdgcn_update_dpp(0, w, 0x00, 0xf, 0xf, false), p1 = (unsigned)__builtin_amdgcn_update_dpp(0, w, 0x55, 0xf, 0xf, false);
;                             const unsigned p2 = (unsigned)__builtin_amdgcn_update_dpp(0, w, 0xaa, 0xf, 0xf, false), p3 = (unsigned)__builtin_amdgcn_update_dpp(0, w, 0xff, 0xf, 0xf, false);
;                             const unsigned t01 = __builtin_amdgcn_perm(p1, p0, sel), t23 = __builtin_amdgcn_perm(p3, p2, sel);
;                             *(unsigned*)(tb_ + (hh * 4 + qi) * 64) = t01 | (t23 << 16); } } }
	v_med3_f32 v34, v83, s33, v217
	v_cvt_pk_fp8_f32 v80, v1, v34 op_sel:[0,0,1]
	v_mov_b32_e32 v1, v35
	v_mov_b32_e32 v34, v35
	v_mov_b32_e32 v81, v35
	v_mov_b32_e32 v82, v35
	v_mov_b32_dpp v1, v80 quad_perm:[0,0,0,0] row_mask:0xf bank_mask:0xf
	v_mov_b32_dpp v34, v80 quad_perm:[1,1,1,1] row_mask:0xf bank_mask:0xf
	v_mov_b32_dpp v81, v80 quad_perm:[2,2,2,2] row_mask:0xf bank_mask:0xf
	v_mov_b32_dpp v82, v80 quad_perm:[3,3,3,3] row_mask:0xf bank_mask:0xf
	v_perm_b32 v1, v34, v1, v157
	v_perm_b32 v34, v82, v81, v157
	v_lshl_or_b32 v1, v34, 16, v1
	v_lshl_add_u64 v[80:81], v[88:89], 0, v[132:133]
	v_pk_mul_f32 v[76:77], v[86:87], v[76:77] op_sel_hi:[0,1]
	global_store_dword v[80:81], v1, off offset:16
	v_med3_f32 v1, v76, s33, v217
	v_med3_f32 v34, v77, s33, v217
	v_mov_b32_e32 v76, v35
	v_cvt_pk_fp8_f32 v76, v1, v34
	v_pk_mul_f32 v[78:79], v[86:87], v[78:79] op_sel_hi:[0,1]
	v_med3_f32 v1, v78, s33, v217
	v_med3_f32 v34, v79, s33, v217
	v_cvt_pk_fp8_f32 v76, v1, v34 op_sel:[0,0,1]
	v_mov_b32_e32 v1, v35
	v_mov_b32_e32 v34, v35
	v_mov_b32_e32 v77, v35
	v_mov_b32_e32 v78, v35
	v_mov_b32_dpp v1, v76 quad_perm:[0,0,0,0] row_mask:0xf bank_mask:0xf
	v_mov_b32_dpp v34, v76 quad_perm:[1,1,1,1] row_mask:0xf bank_mask:0xf
	v_mov_b32_dpp v77, v76 quad_perm:[2,2,2,2] row_mask:0xf bank_mask:0xf
	v_mov_b32_dpp v78, v76 quad_perm:[3,3,3,3] row_mask:0xf bank_mask:0xf
	v_perm_b32 v1, v34, v1, v157
	v_perm_b32 v34, v78, v77, v157
	v_lshl_or_b32 v1, v34, 16, v1
	v_pk_mul_f32 v[72:73], v[86:87], v[72:73] op_sel_hi:[0,1]
	global_store_dword v[80:81], v1, off offset:272
	v_med3_f32 v1, v72, s33, v217
	v_med3_f32 v34, v73, s33, v217
	v_mov_b32_e32 v72, v35
	v_cvt_pk_fp8_f32 v72, v1, v34
	v_pk_mul_f32 v[74:75], v[86:87], v[74:75] op_sel_hi:[0,1]
	v_med3_f32 v1, v74, s33, v217
	v_med3_f32 v34, v75, s33, v217
	v_cvt_pk_fp8_f32 v72, v1, v34 op_sel:[0,0,1]
	v_mov_b32_e32 v1, v35
	v_mov_b32_e32 v34, v35
	v_mov_b32_e32 v73, v35
	v_mov_b32_e32 v74, v35
	v_mov_b32_dpp v1, v72 quad_perm:[0,0,0,0] row_mask:0xf bank_mask:0xf
	v_mov_b32_dpp v34, v72 quad_perm:[1,1,1,1] row_mask:0xf bank_mask:0xf
	v_mov_b32_dpp v73, v72 quad_perm:[2,2,2,2] row_mask:0xf bank_mask:0xf
	v_mov_b32_dpp v74, v72 quad_perm:[3,3,3,3] row_mask:0xf bank_mask:0xf
	v_lshl_add_u64 v[76:77], v[84:85], 0, s[24:25]
	v_perm_b32 v1, v34, v1, v157
	v_perm_b32 v34, v74, v73, v157
	v_lshl_or_b32 v1, v34, 16, v1
	v_lshl_add_u64 v[72:73], v[76:77], 0, v[132:133]
	v_pk_mul_f32 v[68:69], v[86:87], v[68:69] op_sel_hi:[0,1]
	global_store_dword v[72:73], v1, off offset:16
	v_med3_f32 v1, v68, s33, v217
	v_med3_f32 v34, v69, s33, v217
	v_mov_b32_e32 v68, v35
	v_cvt_pk_fp8_f32 v68, v1, v34
	v_pk_mul_f32 v[70:71], v[86:87], v[70:71] op_sel_hi:[0,1]
	v_med3_f32 v1, v70, s33, v217
	v_med3_f32 v34, v71, s33, v217
	v_cvt_pk_fp8_f32 v68, v1, v34 op_sel:[0,0,1]
	v_mov_b32_e32 v1, v35
	v_mov_b32_e32 v34, v35
	v_mov_b32_e32 v69, v35
	v_mov_b32_e32 v70, v35
	v_mov_b32_dpp v1, v68 quad_perm:[0,0,0,0] row_mask:0xf bank_mask:0xf
	v_mov_b32_dpp v34, v68 quad_perm:[1,1,1,1] row_mask:0xf bank_mask:0xf
	v_mov_b32_dpp v69, v68 quad_perm:[2,2,2,2] row_mask:0xf bank_mask:0xf
	v_mov_b32_dpp v70, v68 quad_perm:[3,3,3,3] row_mask:0xf bank_mask:0xf
	v_perm_b32 v1, v34, v1, v157
	v_perm_b32 v34, v70, v69, v157
	v_lshl_or_b32 v1, v34, 16, v1
	global_store_dword v[72:73], v1, off offset:272
	v_cvt_f32_i32_e32 v69, v61
	v_cvt_f32_i32_e32 v68, v60
	s_lshl_b64 s[24:25], s[0:1], 13
	v_lshl_add_u64 v[60:61], v[152:153], 0, s[24:25]
	v_lshl_add_u64 v[60:61], v[60:61], 0, v[132:133]
	s_add_i32 s0, s19, s26
	s_ashr_i32 s1, s0, 31
	s_lshl_b64 s[0:1], s[0:1], 13
	v_mov_b32_e32 v1, v228
	v_mul_f32_e32 v34, v184, v1
	v_pk_mul_f32 v[64:65], v[34:35], v[64:65] op_sel_hi:[0,1]
	v_med3_f32 v1, v64, s33, v217
	v_med3_f32 v64, v65, s33, v217
	v_mov_b32_e32 v65, v35
	v_cvt_pk_fp8_f32 v65, v1, v64
	v_pk_mul_f32 v[66:67], v[34:35], v[66:67] op_sel_hi:[0,1]
	v_med3_f32 v1, v66, s33, v217
	v_med3_f32 v64, v67, s33, v217
	v_cvt_pk_fp8_f32 v65, v1, v64 op_sel:[0,0,1]
	v_mov_b32_e32 v1, v35
	v_mov_b32_e32 v64, v35
	v_mov_b32_e32 v66, v35
	v_mov_b32_e32 v67, v35
	v_mov_b32_dpp v1, v65 quad_perm:[0,0,0,0] row_mask:0xf bank_mask:0xf
	v_mov_b32_dpp v64, v65 quad_perm:[1,1,1,1] row_mask:0xf bank_mask:0xf
	v_mov_b32_dpp v66, v65 quad_perm:[2,2,2,2] row_mask:0xf bank_mask:0xf
	v_mov_b32_dpp v67, v65 quad_perm:[3,3,3,3] row_mask:0xf bank_mask:0xf
	v_perm_b32 v1, v64, v1, v157
	v_perm_b32 v64, v67, v66, v157
	v_lshl_or_b32 v1, v64, 16, v1
	v_pk_mul_f32 v[64:65], v[34:35], v[68:69] op_sel_hi:[0,1]
	global_store_dword v[60:61], v1, off
	v_med3_f32 v1, v64, s33, v217
	v_med3_f32 v64, v65, s33, v217
	v_mov_b32_e32 v65, v35
	v_cvt_pk_fp8_f32 v65, v1, v64
	v_pk_mul_f32 v[62:63], v[34:35], v[62:63] op_sel_hi:[0,1]
	v_med3_f32 v1, v62, s33, v217
	v_med3_f32 v62, v63, s33, v217
	v_cvt_pk_fp8_f32 v65, v1, v62 op_sel:[0,0,1]
	v_mov_b32_e32 v1, v35
	v_mov_b32_e32 v62, v35
	v_mov_b32_e32 v63, v35
	v_mov_b32_e32 v64, v35
	v_mov_b32_dpp v1, v65 quad_perm:[0,0,0,0] row_mask:0xf bank_mask:0xf
	v_mov_b32_dpp v62, v65 quad_perm:[1,1,1,1] row_mask:0xf bank_mask:0xf
	v_mov_b32_dpp v63, v65 quad_perm:[2,2,2,2] row_mask:0xf bank_mask:0xf
	v_mov_b32_dpp v64, v65 quad_perm:[3,3,3,3] row_mask:0xf bank_mask:0xf
	v_perm_b32 v1, v62, v1, v157
	v_perm_b32 v62, v64, v63, v157
	v_lshl_or_b32 v1, v62, 16, v1
	v_pk_mul_f32 v[56:57], v[34:35], v[56:57] op_sel_hi:[0,1]
	global_store_dword v[60:61], v1, off offset:256
	v_med3_f32 v1, v56, s33, v217
	v_med3_f32 v56, v57, s33, v217
	v_mov_b32_e32 v57, v35
	v_cvt_pk_fp8_f32 v57, v1, v56
	v_pk_mul_f32 v[58:59], v[34:35], v[58:59] op_sel_hi:[0,1]
	v_med3_f32 v1, v58, s33, v217
; __device__ __forceinline__ f32x4 tof(const i32x4& a) { return (f32x4){(float)a.x, (float)a.y, (float)a.z, (float)a.w}; }
;     template <class AT> __device__ __forceinline__ void operator()(const AT (&acc)[2][2][4][2], const Unit& u, int wr, int wc, int fr, int fq) const {
;     ...
;             for (int ai = 0; ai < 2; ++ai)
; #pragma unroll
;                 for (int m = 0; m < 4; ++m) { const float rsc = sa[row0 + ai * HALF + m * 16] * sw;
;                     const int tile = (u.pm % 17) * 4 + wr + 2 * ai, pos0 = 32 * (a4 & 1) + 16 * (m >> 1) + 4 * ((2 * m + (a4 >> 1)) & 3);
; #pragma unroll
;                     for (int bj = 0; bj < 2; ++bj) { const f32x4 v0 = tof(acc[ai][bj][m][0]) * rsc, v1 = tof(acc[ai][bj][m][1]) * rsc;
;                         unsigned char* tb_ = vq + ((size_t)((b * nhv + hv0 + bj) * 68 + tile)) * 8192 + (size_t)(wc * 32 + 8 * fql) * 64 + pos0;
; #pragma unroll
;                         for (int hh = 0; hh < 2; ++hh) { const f32x4 vv = hh ? v1 : v0; const int w = (int)pack_f8x4(vv[0], vv[1], vv[2], vv[3], 1.f);
;                             const unsigned p0 = (unsigned)__builtin_amdgcn_update_dpp(0, w, 0x00, 0xf, 0xf, false), p1 = (unsigned)__builtin_amdgcn_update_dpp(0, w, 0x55, 0xf, 0xf, false);
;                             const unsigned p2 = (unsigned)__builtin_amdgcn_update_dpp(0, w, 0xaa, 0xf, 0xf, false), p3 = (unsigned)__builtin_amdgcn_update_dpp(0, w, 0xff, 0xf, 0xf, false);
;                             const unsigned t01 = __builtin_amdgcn_perm(p1, p0, sel), t23 = __builtin_amdgcn_perm(p3, p2, sel);
;                             *(unsigned*)(tb_ + (hh * 4 + qi) * 64) = t01 | (t23 << 16); } } }
	v_med3_f32 v56, v59, s33, v217
	v_cvt_pk_fp8_f32 v57, v1, v56 op_sel:[0,0,1]
	v_cvt_f32_i32_e32 v63, v53
	v_cvt_f32_i32_e32 v62, v52
	v_mov_b32_e32 v1, v35
	v_mov_b32_e32 v56, v35
	v_mov_b32_e32 v58, v35
	v_mov_b32_e32 v59, v35
	v_mov_b32_dpp v1, v57 quad_perm:[0,0,0,0] row_mask:0xf bank_mask:0xf
	v_mov_b32_dpp v56, v57 quad_perm:[1,1,1,1] row_mask:0xf bank_mask:0xf
	v_mov_b32_dpp v58, v57 quad_perm:[2,2,2,2] row_mask:0xf bank_mask:0xf
	v_mov_b32_dpp v59, v57 quad_perm:[3,3,3,3] row_mask:0xf bank_mask:0xf
	v_lshl_add_u64 v[52:53], v[152:153], 0, s[0:1]
	v_perm_b32 v1, v56, v1, v157
	v_perm_b32 v56, v59, v58, v157
	v_lshl_or_b32 v1, v56, 16, v1
	v_lshl_add_u64 v[52:53], v[52:53], 0, v[132:133]
	v_pk_mul_f32 v[56:57], v[34:35], v[62:63] op_sel_hi:[0,1]
	global_store_dword v[52:53], v1, off
	v_pk_mul_f32 v[54:55], v[34:35], v[54:55] op_sel_hi:[0,1]
	v_med3_f32 v1, v56, s33, v217
	v_med3_f32 v34, v57, s33, v217
	v_mov_b32_e32 v56, v35
	v_cvt_pk_fp8_f32 v56, v1, v34
	v_med3_f32 v1, v54, s33, v217
	v_med3_f32 v34, v55, s33, v217
	v_mov_b32_e32 v54, v35
	v_cvt_pk_fp8_f32 v56, v1, v34 op_sel:[0,0,1]
	v_mov_b32_e32 v1, v35
	v_mov_b32_e32 v34, v35
	v_mov_b32_e32 v55, v35
	v_mov_b32_dpp v1, v56 quad_perm:[0,0,0,0] row_mask:0xf bank_mask:0xf
	v_mov_b32_dpp v34, v56 quad_perm:[1,1,1,1] row_mask:0xf bank_mask:0xf
	v_mov_b32_dpp v54, v56 quad_perm:[2,2,2,2] row_mask:0xf bank_mask:0xf
	v_mov_b32_dpp v55, v56 quad_perm:[3,3,3,3] row_mask:0xf bank_mask:0xf
	v_perm_b32 v1, v34, v1, v157
	v_perm_b32 v34, v55, v54, v157
	v_lshl_or_b32 v1, v34, 16, v1
	global_store_dword v[52:53], v1, off offset:256
	v_lshl_add_u64 v[54:55], v[116:117], 0, s[24:25]
	v_mov_b32_e32 v1, v229
	v_mul_f32_e32 v34, v184, v1
	v_pk_mul_f32 v[48:49], v[34:35], v[48:49] op_sel_hi:[0,1]
	v_med3_f32 v1, v48, s33, v217
	v_med3_f32 v48, v49, s33, v217
	v_mov_b32_e32 v49, v35
	v_cvt_pk_fp8_f32 v49, v1, v48
	v_pk_mul_f32 v[50:51], v[34:35], v[50:51] op_sel_hi:[0,1]
	v_med3_f32 v1, v50, s33, v217
	v_med3_f32 v48, v51, s33, v217
	v_cvt_pk_fp8_f32 v49, v1, v48 op_sel:[0,0,1]
	v_mov_b32_e32 v1, v35
	v_mov_b32_e32 v48, v35
	v_mov_b32_e32 v50, v35
	v_mov_b32_e32 v51, v35
	v_mov_b32_dpp v1, v49 quad_perm:[0,0,0,0] row_mask:0xf bank_mask:0xf
	v_mov_b32_dpp v48, v49 quad_perm:[1,1,1,1] row_mask:0xf bank_mask:0xf
	v_mov_b32_dpp v50, v49 quad_perm:[2,2,2,2] row_mask:0xf bank_mask:0xf
	v_mov_b32_dpp v51, v49 quad_perm:[3,3,3,3] row_mask:0xf bank_mask:0xf
	v_perm_b32 v1, v48, v1, v157
	v_perm_b32 v48, v51, v50, v157
	v_lshl_or_b32 v1, v48, 16, v1
	v_lshl_add_u64 v[48:49], v[54:55], 0, v[132:133]
	v_pk_mul_f32 v[44:45], v[34:35], v[44:45] op_sel_hi:[0,1]
	global_store_dword v[48:49], v1, off
	v_med3_f32 v1, v44, s33, v217
	v_med3_f32 v44, v45, s33, v217
	v_mov_b32_e32 v45, v35
	v_cvt_pk_fp8_f32 v45, v1, v44
	v_pk_mul_f32 v[46:47], v[34:35], v[46:47] op_sel_hi:[0,1]
	v_med3_f32 v1, v46, s33, v217
	v_med3_f32 v44, v47, s33, v217
	v_cvt_pk_fp8_f32 v45, v1, v44 op_sel:[0,0,1]
	v_mov_b32_e32 v1, v35
	v_mov_b32_e32 v44, v35
	v_mov_b32_e32 v46, v35
	v_mov_b32_e32 v47, v35
	v_mov_b32_dpp v1, v45 quad_perm:[0,0,0,0] row_mask:0xf bank_mask:0xf
	v_mov_b32_dpp v44, v45 quad_perm:[1,1,1,1] row_mask:0xf bank_mask:0xf
	v_mov_b32_dpp v46, v45 quad_perm:[2,2,2,2] row_mask:0xf bank_mask:0xf
	v_mov_b32_dpp v47, v45 quad_perm:[3,3,3,3] row_mask:0xf bank_mask:0xf
	v_perm_b32 v1, v44, v1, v157
	v_perm_b32 v44, v47, v46, v157
	v_lshl_or_b32 v1, v44, 16, v1
	v_pk_mul_f32 v[40:41], v[34:35], v[40:41] op_sel_hi:[0,1]
	global_store_dword v[48:49], v1, off offset:256
	v_med3_f32 v1, v40, s33, v217
	v_med3_f32 v40, v41, s33, v217
	v_mov_b32_e32 v41, v35
	v_cvt_pk_fp8_f32 v41, v1, v40
	v_pk_mul_f32 v[42:43], v[34:35], v[42:43] op_sel_hi:[0,1]
	v_med3_f32 v1, v42, s33, v217
	v_med3_f32 v40, v43, s33, v217
	v_cvt_pk_fp8_f32 v41, v1, v40 op_sel:[0,0,1]
	v_mov_b32_e32 v1, v35
	v_mov_b32_e32 v40, v35
	v_mov_b32_e32 v42, v35
	v_mov_b32_e32 v43, v35
	v_mov_b32_dpp v1, v41 quad_perm:[0,0,0,0] row_mask:0xf bank_mask:0xf
	v_mov_b32_dpp v40, v41 quad_perm:[1,1,1,1] row_mask:0xf bank_mask:0xf
	v_mov_b32_dpp v42, v41 quad_perm:[2,2,2,2] row_mask:0xf bank_mask:0xf
	v_mov_b32_dpp v43, v41 quad_perm:[3,3,3,3] row_mask:0xf bank_mask:0xf
	v_lshl_add_u64 v[44:45], v[116:117], 0, s[0:1]
	v_perm_b32 v1, v40, v1, v157
	v_perm_b32 v40, v43, v42, v157
	v_lshl_or_b32 v1, v40, 16, v1
	v_lshl_add_u64 v[40:41], v[44:45], 0, v[132:133]
	v_pk_mul_f32 v[36:37], v[34:35], v[36:37] op_sel_hi:[0,1]
	global_store_dword v[40:41], v1, off
	v_pk_mul_f32 v[38:39], v[34:35], v[38:39] op_sel_hi:[0,1]
	v_med3_f32 v1, v36, s33, v217
	v_med3_f32 v34, v37, s33, v217
	v_mov_b32_e32 v36, v35
	v_cvt_pk_fp8_f32 v36, v1, v34
	v_med3_f32 v1, v38, s33, v217
	v_med3_f32 v34, v39, s33, v217
	v_mov_b32_e32 v37, v35
	v_cvt_pk_fp8_f32 v36, v1, v34 op_sel:[0,0,1]
	v_mov_b32_e32 v1, v35
	v_mov_b32_e32 v34, v35
	v_mov_b32_e32 v38, v35
	v_mov_b32_dpp v1, v36 quad_perm:[0,0,0,0] row_mask:0xf bank_mask:0xf
	v_mov_b32_dpp v34, v36 quad_perm:[1,1,1,1] row_mask:0xf bank_mask:0xf
	v_mov_b32_dpp v37, v36 quad_perm:[2,2,2,2] row_mask:0xf bank_mask:0xf
	v_mov_b32_dpp v38, v36 quad_perm:[3,3,3,3] row_mask:0xf bank_mask:0xf
	v_perm_b32 v1, v34, v1, v157
	v_perm_b32 v34, v38, v37, v157
	v_lshl_or_b32 v1, v34, 16, v1
	global_store_dword v[40:41], v1, off offset:256
	v_mov_b32_e32 v1, v230
	v_mul_f32_e32 v34, v184, v1
	v_pk_mul_f32 v[30:31], v[34:35], v[30:31] op_sel_hi:[0,1]
	v_med3_f32 v1, v30, s33, v217
	v_med3_f32 v30, v31, s33, v217
	v_mov_b32_e32 v31, v35
	v_cvt_pk_fp8_f32 v31, v1, v30
	v_pk_mul_f32 v[32:33], v[34:35], v[32:33] op_sel_hi:[0,1]
	v_med3_f32 v1, v32, s33, v217
	v_med3_f32 v30, v33, s33, v217
; __device__ __forceinline__ f32x4 tof(const i32x4& a) { return (f32x4){(float)a.x, (float)a.y, (float)a.z, (float)a.w}; }
;     template <class AT> __device__ __forceinline__ void operator()(const AT (&acc)[2][2][4][2], const Unit& u, int wr, int wc, int fr, int fq) const {
;     ...
;             for (int ai = 0; ai < 2; ++ai)
; #pragma unroll
;                 for (int m = 0; m < 4; ++m) { const float rsc = sa[row0 + ai * HALF + m * 16] * sw;
;                     const int tile = (u.pm % 17) * 4 + wr + 2 * ai, pos0 = 32 * (a4 & 1) + 16 * (m >> 1) + 4 * ((2 * m + (a4 >> 1)) & 3);
; #pragma unroll
;                     for (int bj = 0; bj < 2; ++bj) { const f32x4 v0 = tof(acc[ai][bj][m][0]) * rsc, v1 = tof(acc[ai][bj][m][1]) * rsc;
;                         unsigned char* tb_ = vq + ((size_t)((b * nhv + hv0 + bj) * 68 + tile)) * 8192 + (size_t)(wc * 32 + 8 * fql) * 64 + pos0;
; #pragma unroll
;                         for (int hh = 0; hh < 2; ++hh) { const f32x4 vv = hh ? v1 : v0; const int w = (int)pack_f8x4(vv[0], vv[1], vv[2], vv[3], 1.f);
;                             const unsigned p0 = (unsigned)__builtin_amdgcn_update_dpp(0, w, 0x00, 0xf, 0xf, false), p1 = (unsigned)__builtin_amdgcn_update_dpp(0, w, 0x55, 0xf, 0xf, false);
;                             const unsigned p2 = (unsigned)__builtin_amdgcn_update_dpp(0, w, 0xaa, 0xf, 0xf, false), p3 = (unsigned)__builtin_amdgcn_update_dpp(0, w, 0xff, 0xf, 0xf, false);
;                             const unsigned t01 = __builtin_amdgcn_perm(p1, p0, sel), t23 = __builtin_amdgcn_perm(p3, p2, sel);
;                             *(unsigned*)(tb_ + (hh * 4 + qi) * 64) = t01 | (t23 << 16); } } }
	v_cvt_pk_fp8_f32 v31, v1, v30 op_sel:[0,0,1]
	v_mov_b32_e32 v1, v35
	v_mov_b32_e32 v30, v35
	v_mov_b32_e32 v32, v35
	v_mov_b32_e32 v33, v35
	v_mov_b32_dpp v1, v31 quad_perm:[0,0,0,0] row_mask:0xf bank_mask:0xf
	v_mov_b32_dpp v30, v31 quad_perm:[1,1,1,1] row_mask:0xf bank_mask:0xf
	v_mov_b32_dpp v32, v31 quad_perm:[2,2,2,2] row_mask:0xf bank_mask:0xf
	v_mov_b32_dpp v33, v31 quad_perm:[3,3,3,3] row_mask:0xf bank_mask:0xf
	v_perm_b32 v1, v30, v1, v157
	v_perm_b32 v30, v33, v32, v157
	v_lshl_or_b32 v1, v30, 16, v1
	v_pk_mul_f32 v[26:27], v[34:35], v[26:27] op_sel_hi:[0,1]
	global_store_dword v[60:61], v1, off offset:16
	v_med3_f32 v1, v26, s33, v217
	v_med3_f32 v26, v27, s33, v217
	v_mov_b32_e32 v27, v35
	v_cvt_pk_fp8_f32 v27, v1, v26
	v_pk_mul_f32 v[28:29], v[34:35], v[28:29] op_sel_hi:[0,1]
	v_med3_f32 v1, v28, s33, v217
	v_med3_f32 v26, v29, s33, v217
	v_cvt_pk_fp8_f32 v27, v1, v26 op_sel:[0,0,1]
	v_mov_b32_e32 v1, v35
	v_mov_b32_e32 v26, v35
	v_mov_b32_e32 v28, v35
	v_mov_b32_e32 v29, v35
	v_mov_b32_dpp v1, v27 quad_perm:[0,0,0,0] row_mask:0xf bank_mask:0xf
	v_mov_b32_dpp v26, v27 quad_perm:[1,1,1,1] row_mask:0xf bank_mask:0xf
	v_mov_b32_dpp v28, v27 quad_perm:[2,2,2,2] row_mask:0xf bank_mask:0xf
	v_mov_b32_dpp v29, v27 quad_perm:[3,3,3,3] row_mask:0xf bank_mask:0xf
	v_perm_b32 v1, v26, v1, v157
	v_perm_b32 v26, v29, v28, v157
	v_lshl_or_b32 v1, v26, 16, v1
	v_pk_mul_f32 v[22:23], v[34:35], v[22:23] op_sel_hi:[0,1]
	global_store_dword v[60:61], v1, off offset:272
	v_med3_f32 v1, v22, s33, v217
	v_med3_f32 v22, v23, s33, v217
	v_mov_b32_e32 v23, v35
	v_cvt_pk_fp8_f32 v23, v1, v22
	v_pk_mul_f32 v[24:25], v[34:35], v[24:25] op_sel_hi:[0,1]
	v_med3_f32 v1, v24, s33, v217
	v_med3_f32 v22, v25, s33, v217
	v_cvt_pk_fp8_f32 v23, v1, v22 op_sel:[0,0,1]
	v_mov_b32_e32 v1, v35
	v_mov_b32_e32 v22, v35
	v_mov_b32_e32 v24, v35
	v_mov_b32_e32 v25, v35
	v_mov_b32_dpp v1, v23 quad_perm:[0,0,0,0] row_mask:0xf bank_mask:0xf
	v_mov_b32_dpp v22, v23 quad_perm:[1,1,1,1] row_mask:0xf bank_mask:0xf
	v_mov_b32_dpp v24, v23 quad_perm:[2,2,2,2] row_mask:0xf bank_mask:0xf
	v_mov_b32_dpp v25, v23 quad_perm:[3,3,3,3] row_mask:0xf bank_mask:0xf
	v_perm_b32 v1, v22, v1, v157
	v_perm_b32 v22, v25, v24, v157
	v_lshl_or_b32 v1, v22, 16, v1
	v_pk_mul_f32 v[18:19], v[34:35], v[18:19] op_sel_hi:[0,1]
	global_store_dword v[52:53], v1, off offset:16
	v_med3_f32 v1, v18, s33, v217
	v_med3_f32 v18, v19, s33, v217
	v_mov_b32_e32 v19, v35
	v_cvt_pk_fp8_f32 v19, v1, v18
	v_pk_mul_f32 v[20:21], v[34:35], v[20:21] op_sel_hi:[0,1]
	v_med3_f32 v1, v20, s33, v217
	v_med3_f32 v18, v21, s33, v217
	v_cvt_pk_fp8_f32 v19, v1, v18 op_sel:[0,0,1]
	v_mov_b32_e32 v1, v35
	v_mov_b32_e32 v18, v35
	v_mov_b32_e32 v20, v35
	v_mov_b32_e32 v21, v35
	v_mov_b32_dpp v1, v19 quad_perm:[0,0,0,0] row_mask:0xf bank_mask:0xf
	v_mov_b32_dpp v18, v19 quad_perm:[1,1,1,1] row_mask:0xf bank_mask:0xf
	v_mov_b32_dpp v20, v19 quad_perm:[2,2,2,2] row_mask:0xf bank_mask:0xf
	v_mov_b32_dpp v21, v19 quad_perm:[3,3,3,3] row_mask:0xf bank_mask:0xf
	v_perm_b32 v1, v18, v1, v157
	v_perm_b32 v18, v21, v20, v157
	v_lshl_or_b32 v1, v18, 16, v1
	v_lshl_add_u64 v[20:21], v[84:85], 0, s[24:25]
	global_store_dword v[52:53], v1, off offset:272
	v_mov_b32_e32 v18, v231
	v_mul_f32_e32 v18, v184, v18
	v_pk_mul_f32 v[14:15], v[18:19], v[14:15] op_sel_hi:[0,1]
	v_med3_f32 v1, v14, s33, v217
	v_med3_f32 v14, v15, s33, v217
	v_mov_b32_e32 v15, v35
	v_cvt_pk_fp8_f32 v15, v1, v14
	v_pk_mul_f32 v[16:17], v[18:19], v[16:17] op_sel_hi:[0,1]
	v_med3_f32 v1, v16, s33, v217
	v_med3_f32 v14, v17, s33, v217
	v_cvt_pk_fp8_f32 v15, v1, v14 op_sel:[0,0,1]
	v_mov_b32_e32 v1, v35
	v_mov_b32_e32 v14, v35
	v_mov_b32_e32 v16, v35
	v_mov_b32_e32 v17, v35
	v_mov_b32_dpp v1, v15 quad_perm:[0,0,0,0] row_mask:0xf bank_mask:0xf
	v_mov_b32_dpp v14, v15 quad_perm:[1,1,1,1] row_mask:0xf bank_mask:0xf
	v_mov_b32_dpp v16, v15 quad_perm:[2,2,2,2] row_mask:0xf bank_mask:0xf
	v_mov_b32_dpp v17, v15 quad_perm:[3,3,3,3] row_mask:0xf bank_mask:0xf
	v_perm_b32 v1, v14, v1, v157
	v_perm_b32 v14, v17, v16, v157
	v_lshl_or_b32 v1, v14, 16, v1
	v_lshl_add_u64 v[14:15], v[20:21], 0, v[132:133]
	v_pk_mul_f32 v[10:11], v[18:19], v[10:11] op_sel_hi:[0,1]
	global_store_dword v[14:15], v1, off offset:16
	v_med3_f32 v1, v10, s33, v217
	v_med3_f32 v10, v11, s33, v217
	v_mov_b32_e32 v11, v35
	v_cvt_pk_fp8_f32 v11, v1, v10
	v_pk_mul_f32 v[12:13], v[18:19], v[12:13] op_sel_hi:[0,1]
	v_med3_f32 v1, v12, s33, v217
	v_med3_f32 v10, v13, s33, v217
	v_cvt_pk_fp8_f32 v11, v1, v10 op_sel:[0,0,1]
	v_mov_b32_e32 v1, v35
	v_mov_b32_e32 v10, v35
	v_mov_b32_e32 v12, v35
	v_mov_b32_e32 v13, v35
	v_mov_b32_dpp v1, v11 quad_perm:[0,0,0,0] row_mask:0xf bank_mask:0xf
	v_mov_b32_dpp v10, v11 quad_perm:[1,1,1,1] row_mask:0xf bank_mask:0xf
	v_mov_b32_dpp v12, v11 quad_perm:[2,2,2,2] row_mask:0xf bank_mask:0xf
	v_mov_b32_dpp v13, v11 quad_perm:[3,3,3,3] row_mask:0xf bank_mask:0xf
	v_perm_b32 v1, v10, v1, v157
	v_perm_b32 v10, v13, v12, v157
	v_lshl_or_b32 v1, v10, 16, v1
	v_pk_mul_f32 v[6:7], v[18:19], v[6:7] op_sel_hi:[0,1]
	global_store_dword v[14:15], v1, off offset:272
	v_med3_f32 v1, v6, s33, v217
	v_med3_f32 v6, v7, s33, v217
	v_mov_b32_e32 v7, v35
	v_cvt_pk_fp8_f32 v7, v1, v6
	v_pk_mul_f32 v[8:9], v[18:19], v[8:9] op_sel_hi:[0,1]
	v_med3_f32 v1, v8, s33, v217
	v_med3_f32 v6, v9, s33, v217
	v_cvt_pk_fp8_f32 v7, v1, v6 op_sel:[0,0,1]
	v_mov_b32_e32 v1, v35
	v_mov_b32_e32 v6, v35
	v_mov_b32_e32 v8, v35
	v_mov_b32_e32 v9, v35
	v_mov_b32_dpp v1, v7 quad_perm:[0,0,0,0] row_mask:0xf bank_mask:0xf
	v_mov_b32_dpp v6, v7 quad_perm:[1,1,1,1] row_mask:0xf bank_mask:0xf
	v_mov_b32_dpp v8, v7 quad_perm:[2,2,2,2] row_mask:0xf bank_mask:0xf
	v_mov_b32_dpp v9, v7 quad_perm:[3,3,3,3] row_mask:0xf bank_mask:0xf
	v_lshl_add_u64 v[10:11], v[84:85], 0, s[0:1]
	v_perm_b32 v1, v6, v1, v157
	v_perm_b32 v6, v9, v8, v157
	v_lshl_or_b32 v1, v6, 16, v1
	v_lshl_add_u64 v[6:7], v[10:11], 0, v[132:133]
	v_pk_mul_f32 v[2:3], v[18:19], v[2:3] op_sel_hi:[0,1]
	global_store_dword v[6:7], v1, off offset:16
	v_med3_f32 v1, v2, s33, v217
	v_med3_f32 v2, v3, s33, v217
	v_mov_b32_e32 v3, v35
	v_cvt_pk_fp8_f32 v3, v1, v2
	v_pk_mul_f32 v[4:5], v[18:19], v[4:5] op_sel_hi:[0,1]
	v_med3_f32 v1, v4, s33, v217
	v_med3_f32 v2, v5, s33, v217
	v_cvt_pk_fp8_f32 v3, v1, v2 op_sel:[0,0,1]
	v_mov_b32_e32 v1, v35
	v_mov_b32_e32 v2, v35
	v_mov_b32_e32 v4, v35
	v_mov_b32_e32 v5, v35
	v_mov_b32_dpp v1, v3 quad_perm:[0,0,0,0] row_mask:0xf bank_mask:0xf
	v_mov_b32_dpp v2, v3 quad_perm:[1,1,1,1] row_mask:0xf bank_mask:0xf
	v_mov_b32_dpp v4, v3 quad_perm:[2,2,2,2] row_mask:0xf bank_mask:0xf
	v_mov_b32_dpp v5, v3 quad_perm:[3,3,3,3] row_mask:0xf bank_mask:0xf
	v_perm_b32 v1, v2, v1, v157
	v_perm_b32 v2, v5, v4, v157
	v_lshl_or_b32 v1, v2, 16, v1
	global_store_dword v[6:7], v1, off offset:272
